# strategy 7.4: one static s_setprio 1 for the younger half (waves 4-7) before each attention tile loop, reset at phase end; base = v52 + phase_final batched loads (GEMM per-phase flips kept)
# baseline (speedup 1.0000x reference)
.LBB0_804:
	s_bfe_u32 s0, s66, 0x20001
	s_bfe_u32 s1, s78, 0x10007
	s_lshl_b32 s12, s1, 8
	s_lshl_b32 s44, s0, 9
	s_or_b32 s48, s44, s12
	s_mulk_i32 s0, 0x180
	s_mul_i32 s12, s1, 0xc0
	s_add_i32 s0, s0, s12
	s_lshl_b32 s50, s0, 1
	s_ashr_i32 s0, s78, 4
	s_lshl_b32 s12, s78, 1
	s_and_b32 s0, s0, -16
	s_and_b32 s44, s12, 8
	s_bfe_u32 s80, s78, 0x40003
	s_or_b32 s0, s0, s44
	s_xor_b32 s49, s80, 31
	s_ashr_i32 s0, s0, 3
	s_and_b32 s12, s12, 6
	s_lshl_b32 s83, s49, 8
	s_or_b32 s46, s12, s1
	s_ashr_i32 s1, s0, 31
	s_add_i32 s84, s83, s63
	s_lshr_b32 s81, s78, 3
	v_mov_b32_e32 v172, v1
	s_lshl_b64 s[52:53], s[0:1], 13
	s_ashr_i32 s12, s84, 31
	s_add_u32 s54, s52, s84
	v_and_b32_e32 v168, 31, v172
	v_or_b32_e32 v38, s54, v168
	s_addc_u32 s55, s53, s12
	v_mad_u64_u32 v[2:3], s[44:45], v38, s68, v[146:147]
	s_mul_i32 s82, s46, 0xc0
	v_bfe_u32 v173, v172, 5, 1
	v_mad_i32_i24 v3, s55, v162, v3
	s_lshl_b32 s12, s82, 1
	v_lshl_add_u64 v[2:3], v[2:3], 0, s[12:13]
	v_lshlrev_b32_e32 v148, 4, v173
	v_lshl_add_u64 v[40:41], v[2:3], 0, v[148:149]
	global_load_dwordx4 v[6:9], v[40:41], off
	global_load_dwordx4 v[14:17], v[40:41], off offset:32
	global_load_dwordx4 v[30:33], v[40:41], off offset:64
	global_load_dwordx4 v[34:37], v[40:41], off offset:96
	global_load_dwordx4 v[50:53], v[40:41], off offset:128
	global_load_dwordx4 v[26:29], v[40:41], off offset:160
	global_load_dwordx4 v[22:25], v[40:41], off offset:192
	global_load_dwordx4 v[18:21], v[40:41], off offset:224
	global_load_dwordx4 v[10:13], v[40:41], off offset:256
	global_load_dwordx4 v[42:45], v[40:41], off offset:288
	s_waitcnt lgkmcnt(0)
	global_load_dwordx4 v[2:5], v[40:41], off offset:320
	global_load_dwordx4 v[46:49], v[40:41], off offset:352
	v_and_b32_e32 v40, 32, v172
	v_mov_b32_e32 v39, s55
	s_mul_i32 s86, s0, 0x1800000
	s_mul_hi_i32 s51, s0, 0x1800000
	s_add_u32 s44, s33, s86
	s_addc_u32 s45, s58, s51
	s_lshl_b64 s[56:57], s[0:1], 24
	s_lshl_b32 s79, s46, 7
	s_add_u32 s44, s44, s12
	s_addc_u32 s45, s45, 0
	s_mov_b32 m0, s71
	s_add_u32 s0, s59, s56
	s_addc_u32 s1, s60, s57
	s_lshl_b32 s12, s46, 8
	s_add_u32 s46, s0, s12
	s_addc_u32 s47, s1, 0
	s_lshl_b32 s85, s49, 2
	s_add_i32 s85, s85, 4
	s_or_b32 s48, s56, s48
	s_add_u32 s48, s48, 0x29020000
	s_addc_u32 s49, s57, 0
	s_or_b32 s50, s86, s50
	s_add_u32 s50, s50, 0x23030000
	s_addc_u32 s51, s51, 0
	s_mov_b32 s12, 1
	s_movk_i32 s86, 0xff00
	s_waitcnt vmcnt(0)
	v_lshlrev_b32_e32 v227, 16, v26
	v_lshlrev_b32_e32 v177, 16, v6
	v_and_b32_e32 v174, 0xffff0000, v6
	v_lshlrev_b32_e32 v170, 16, v7
	v_and_b32_e32 v167, 0xffff0000, v7
	v_lshlrev_b32_e32 v180, 16, v8
	v_and_b32_e32 v176, 0xffff0000, v8
	v_lshlrev_b32_e32 v171, 16, v9
	v_and_b32_e32 v169, 0xffff0000, v9
	v_lshlrev_b32_e32 v185, 16, v14
	v_and_b32_e32 v182, 0xffff0000, v14
	v_lshlrev_b32_e32 v179, 16, v15
	v_and_b32_e32 v175, 0xffff0000, v15
	v_lshlrev_b32_e32 v187, 16, v16
	v_and_b32_e32 v183, 0xffff0000, v16
	v_lshlrev_b32_e32 v181, 16, v17
	v_and_b32_e32 v178, 0xffff0000, v17
	v_lshlrev_b32_e32 v201, 16, v34
	v_and_b32_e32 v198, 0xffff0000, v34
	v_lshlrev_b32_e32 v196, 16, v35
	v_and_b32_e32 v192, 0xffff0000, v35
	v_lshlrev_b32_e32 v202, 16, v36
	v_and_b32_e32 v199, 0xffff0000, v36
	v_lshlrev_b32_e32 v197, 16, v37
	v_and_b32_e32 v194, 0xffff0000, v37
	v_and_b32_e32 v228, 0xffff0000, v26
	global_load_dwordx4 v[142:145], v40, s[4:5] offset:704
	global_load_dwordx4 v[130:133], v40, s[4:5] offset:720
	global_load_dwordx4 v[6:9], v40, s[4:5] offset:592
	v_lshlrev_b32_e32 v229, 16, v27
	global_load_dwordx4 v[14:17], v40, s[4:5] offset:576
	v_and_b32_e32 v230, 0xffff0000, v27
	v_lshlrev_b32_e32 v231, 16, v28
	v_and_b32_e32 v232, 0xffff0000, v28
	v_lshlrev_b32_e32 v233, 16, v29
	v_and_b32_e32 v234, 0xffff0000, v29
	global_load_dwordx4 v[34:37], v40, s[4:5] offset:640
	global_load_dwordx4 v[156:159], v40, s[4:5] offset:656
	global_load_dwordx4 v[26:29], v40, s[4:5] offset:528
	v_mul_f32_e32 v209, v174, v174
	v_fmac_f32_e32 v209, v177, v177
	v_fmac_f32_e32 v209, v170, v170
	v_fmac_f32_e32 v209, v167, v167
	v_fmac_f32_e32 v209, v180, v180
	v_fmac_f32_e32 v209, v176, v176
	v_fmac_f32_e32 v209, v171, v171
	v_fmac_f32_e32 v209, v169, v169
	v_fmac_f32_e32 v209, v185, v185
	v_lshlrev_b32_e32 v193, 16, v30
	v_and_b32_e32 v190, 0xffff0000, v30
	v_lshlrev_b32_e32 v188, 16, v31
	v_and_b32_e32 v184, 0xffff0000, v31
	v_lshlrev_b32_e32 v195, 16, v32
	v_and_b32_e32 v191, 0xffff0000, v32
	v_lshlrev_b32_e32 v189, 16, v33
	v_and_b32_e32 v186, 0xffff0000, v33
	v_fmac_f32_e32 v209, v182, v182
	global_load_dwordx4 v[30:33], v40, s[4:5] offset:512
	v_fmac_f32_e32 v209, v179, v179
	v_fmac_f32_e32 v209, v175, v175
	v_fmac_f32_e32 v209, v187, v187
	v_fmac_f32_e32 v209, v183, v183
	v_fmac_f32_e32 v209, v181, v181
	v_fmac_f32_e32 v209, v178, v178
	v_fmac_f32_e32 v209, v193, v193
	v_fmac_f32_e32 v209, v190, v190
	v_fmac_f32_e32 v209, v188, v188
	v_fmac_f32_e32 v209, v184, v184
	v_fmac_f32_e32 v209, v195, v195
	v_fmac_f32_e32 v209, v191, v191
	v_fmac_f32_e32 v209, v189, v189
	v_fmac_f32_e32 v209, v186, v186
	v_fmac_f32_e32 v209, v201, v201
	v_fmac_f32_e32 v209, v198, v198
	v_fmac_f32_e32 v209, v196, v196
	v_fmac_f32_e32 v209, v192, v192
	v_fmac_f32_e32 v209, v202, v202
	v_fmac_f32_e32 v209, v199, v199
	v_fmac_f32_e32 v209, v197, v197
	v_lshlrev_b32_e32 v207, 16, v50
	v_fmac_f32_e32 v209, v194, v194
	v_and_b32_e32 v205, 0xffff0000, v50
	v_fmac_f32_e32 v209, v207, v207
	v_lshlrev_b32_e32 v203, 16, v51
	v_fmac_f32_e32 v209, v205, v205
	v_and_b32_e32 v200, 0xffff0000, v51
	v_fmac_f32_e32 v209, v203, v203
	v_lshlrev_b32_e32 v208, 16, v52
	v_fmac_f32_e32 v209, v200, v200
	v_and_b32_e32 v206, 0xffff0000, v52
	v_fmac_f32_e32 v209, v208, v208
	v_lshlrev_b32_e32 v204, 16, v53
	v_fmac_f32_e32 v209, v206, v206
	v_and_b32_e32 v226, 0xffff0000, v53
	v_fmac_f32_e32 v209, v204, v204
	v_fmac_f32_e32 v209, v226, v226
	v_fmac_f32_e32 v209, v227, v227
	v_fmac_f32_e32 v209, v228, v228
	v_fmac_f32_e32 v209, v229, v229
	v_fmac_f32_e32 v209, v230, v230
	global_load_dwordx4 v[110:113], v40, s[4:5] offset:16
	global_load_dwordx4 v[114:117], v40, s[4:5]
	global_load_dwordx4 v[102:105], v40, s[4:5] offset:80
	global_load_dwordx4 v[106:109], v40, s[4:5] offset:64
	global_load_dwordx4 v[94:97], v40, s[4:5] offset:144
	global_load_dwordx4 v[98:101], v40, s[4:5] offset:128
	global_load_dwordx4 v[86:89], v40, s[4:5] offset:208
	global_load_dwordx4 v[90:93], v40, s[4:5] offset:192
	global_load_dwordx4 v[78:81], v40, s[4:5] offset:272
	global_load_dwordx4 v[82:85], v40, s[4:5] offset:256
	global_load_dwordx4 v[70:73], v40, s[4:5] offset:336
	global_load_dwordx4 v[74:77], v40, s[4:5] offset:320
	global_load_dwordx4 v[62:65], v40, s[4:5] offset:400
	global_load_dwordx4 v[66:69], v40, s[4:5] offset:384
	global_load_dwordx4 v[54:57], v40, s[4:5] offset:464
	global_load_dwordx4 v[58:61], v40, s[4:5] offset:448
	v_fmac_f32_e32 v209, v231, v231
	v_fmac_f32_e32 v209, v232, v232
	v_fmac_f32_e32 v209, v233, v233
	v_fmac_f32_e32 v209, v234, v234
	s_waitcnt vmcnt(29)
	v_lshlrev_b32_e32 v235, 16, v22
	v_and_b32_e32 v236, 0xffff0000, v22
	v_fmac_f32_e32 v209, v235, v235
	v_lshlrev_b32_e32 v237, 16, v23
	v_fmac_f32_e32 v209, v236, v236
	v_and_b32_e32 v238, 0xffff0000, v23
	v_fmac_f32_e32 v209, v237, v237
	v_lshlrev_b32_e32 v239, 16, v24
	v_fmac_f32_e32 v209, v238, v238
	v_and_b32_e32 v240, 0xffff0000, v24
	v_fmac_f32_e32 v209, v239, v239
	v_lshlrev_b32_e32 v241, 16, v25
	v_fmac_f32_e32 v209, v240, v240
	v_and_b32_e32 v242, 0xffff0000, v25
	v_fmac_f32_e32 v209, v241, v241
	v_fmac_f32_e32 v209, v242, v242
	s_waitcnt vmcnt(28)
	v_lshlrev_b32_e32 v243, 16, v18
	v_and_b32_e32 v244, 0xffff0000, v18
	v_fmac_f32_e32 v209, v243, v243
	v_lshlrev_b32_e32 v245, 16, v19
	v_fmac_f32_e32 v209, v244, v244
	v_and_b32_e32 v246, 0xffff0000, v19
	v_fmac_f32_e32 v209, v245, v245
	v_lshlrev_b32_e32 v247, 16, v20
	v_fmac_f32_e32 v209, v246, v246
	v_and_b32_e32 v248, 0xffff0000, v20
	v_fmac_f32_e32 v209, v247, v247
	v_lshlrev_b32_e32 v249, 16, v21
	v_fmac_f32_e32 v209, v248, v248
	v_and_b32_e32 v250, 0xffff0000, v21
	v_fmac_f32_e32 v209, v249, v249
	s_waitcnt vmcnt(27)
	v_lshlrev_b32_e32 v223, 16, v10
	s_waitcnt vmcnt(25)
	v_lshlrev_b32_e32 v222, 16, v2
	v_fmac_f32_e32 v209, v250, v250
	s_waitcnt vmcnt(18)
	v_mov_b32_e32 v150, v158
	v_mov_b32_e32 v158, v156
	v_lshlrev_b32_e32 v156, 16, v3
	v_and_b32_e32 v160, 0xffff0000, v3
	v_and_b32_e32 v225, 0xffff0000, v10
	v_and_b32_e32 v224, 0xffff0000, v2
	v_mul_f32_e32 v2, v222, v222
	v_mul_f32_e32 v3, v223, v223
	v_mov_b32_e32 v134, v144
	v_mov_b32_e32 v140, v142
	v_lshlrev_b32_e32 v142, 16, v5
	s_waitcnt vmcnt(17)
	v_mov_b32_e32 v151, v28
	v_and_b32_e32 v144, 0xffff0000, v5
	v_mov_b32_e32 v28, v159
	v_lshlrev_b32_e32 v152, 16, v4
	v_mov_b32_e32 v159, v26
	v_and_b32_e32 v154, 0xffff0000, v4
	v_mov_b32_e32 v26, v157
	v_lshlrev_b32_e32 v157, 16, v11
	v_add_f32_e32 v3, v3, v209
	v_mul_f32_e32 v4, v224, v224
	v_mul_f32_e32 v5, v225, v225
	v_lshlrev_b32_e32 v119, 16, v45
	v_and_b32_e32 v121, 0xffff0000, v45
	v_lshlrev_b32_e32 v125, 16, v44
	v_and_b32_e32 v127, 0xffff0000, v44
	v_mul_f32_e32 v44, v156, v156
	v_mul_f32_e32 v45, v157, v157
	v_and_b32_e32 v161, 0xffff0000, v11
	v_add_f32_e32 v3, v5, v3
	v_mov_b32_e32 v122, v132
	v_mov_b32_e32 v128, v130
	v_lshlrev_b32_e32 v130, 16, v47
	v_and_b32_e32 v132, 0xffff0000, v47
	v_lshlrev_b32_e32 v136, 16, v46
	v_and_b32_e32 v138, 0xffff0000, v46
	v_lshlrev_b32_e32 v153, 16, v12
	v_mul_f32_e32 v46, v160, v160
	v_mul_f32_e32 v47, v161, v161
	v_add_f32_e32 v3, v45, v3
	v_mov_b32_e32 v123, v8
	v_mov_b32_e32 v8, v133
	v_mov_b32_e32 v129, v6
	v_mov_b32_e32 v6, v131
	v_lshlrev_b32_e32 v131, 16, v43
	v_and_b32_e32 v133, 0xffff0000, v43
	v_lshlrev_b32_e32 v137, 16, v42
	v_and_b32_e32 v139, 0xffff0000, v42
	v_mul_f32_e32 v42, v152, v152
	v_mul_f32_e32 v43, v153, v153
	v_and_b32_e32 v155, 0xffff0000, v12
	v_add_f32_e32 v3, v47, v3
	v_mov_b32_e32 v141, v14
	v_mov_b32_e32 v14, v143
	v_lshlrev_b32_e32 v143, 16, v13
	v_mul_f32_e32 v220, v154, v154
	v_mul_f32_e32 v221, v155, v155
	v_add_f32_e32 v3, v43, v3
	v_mov_b32_e32 v135, v16
	v_mov_b32_e32 v16, v145
	v_mul_f32_e32 v216, v142, v142
	v_mul_f32_e32 v217, v143, v143
	v_and_b32_e32 v145, 0xffff0000, v13
	v_add_f32_e32 v3, v221, v3
	v_mul_f32_e32 v218, v144, v144
	v_mul_f32_e32 v219, v145, v145
	v_add_f32_e32 v3, v217, v3
	v_mul_f32_e32 v212, v136, v136
	v_mul_f32_e32 v213, v137, v137
	v_add_f32_e32 v3, v219, v3
	v_mul_f32_e32 v214, v138, v138
	v_mul_f32_e32 v215, v139, v139
	v_add_f32_e32 v3, v213, v3
	v_add_f32_e32 v3, v215, v3
	v_fmac_f32_e32 v3, v131, v131
	v_fmac_f32_e32 v3, v133, v133
	v_fmac_f32_e32 v3, v125, v125
	v_fmac_f32_e32 v3, v127, v127
	v_fmac_f32_e32 v3, v119, v119
	v_fmac_f32_e32 v3, v121, v121
	v_add_f32_e32 v2, v2, v3
	v_add_f32_e32 v43, v4, v2
	v_add_f32_e32 v43, v44, v43
	v_add_f32_e32 v43, v46, v43
	v_add_f32_e32 v209, v42, v43
	v_add_f32_e32 v209, v220, v209
	v_add_f32_e32 v209, v216, v209
	v_add_f32_e32 v209, v218, v209
	v_mov_b32_e32 v218, v132
	v_mov_b32_e32 v219, v130
	v_add_f32_e32 v209, v212, v209
	v_lshlrev_b64 v[18:19], 8, v[38:39]
	v_lshlrev_b32_e32 v124, 16, v48
	v_and_b32_e32 v126, 0xffff0000, v48
	v_mul_f32_e32 v218, v218, v218
	v_mul_f32_e32 v219, v219, v219
	s_waitcnt vmcnt(16)
	v_mov_b32_e32 v213, v32
	v_add_f32_e32 v32, v214, v209
	v_lshl_add_u64 v[18:19], s[10:11], 0, v[18:19]
	v_lshlrev_b32_e32 v20, 6, v173
	v_mov_b32_e32 v21, v149
	v_mov_b32_e32 v216, v126
	v_mov_b32_e32 v217, v124
	v_add_f32_e32 v32, v219, v32
	v_lshl_add_u64 v[210:211], v[18:19], 0, v[20:21]
	v_lshlrev_b32_e32 v118, 16, v49
	v_and_b32_e32 v120, 0xffff0000, v49
	v_mul_f32_e32 v216, v216, v216
	v_mul_f32_e32 v217, v217, v217
	v_add_f32_e32 v32, v218, v32
	global_load_dwordx4 v[18:21], v[210:211], off offset:48
	global_load_dwordx4 v[22:25], v[210:211], off offset:32
	global_load_dwordx4 v[38:41], v[210:211], off offset:16
	global_load_dwordx4 v[50:53], v[210:211], off
	global_load_dwordx4 v[2:5], v[210:211], off offset:176
	global_load_dwordx4 v[10:13], v[210:211], off offset:160
	global_load_dwordx4 v[42:45], v[210:211], off offset:144
	global_load_dwordx4 v[46:49], v[210:211], off offset:128
	v_mov_b32_e32 v210, v120
	v_mov_b32_e32 v211, v118
	v_add_f32_e32 v32, v217, v32
	v_mul_f32_e32 v210, v210, v210
	v_mul_f32_e32 v211, v211, v211
	v_add_f32_e32 v32, v216, v32
	v_add_f32_e32 v32, v211, v32
	v_add_f32_e32 v32, v210, v32
	v_mov_b32_e32 v212, v36
	v_mov_b32_e32 v36, v32
	s_nop 1
	v_permlane32_swap_b32_e32 v32, v36
	v_add_f32_e32 v32, v32, v36
	v_fmamk_f32 v32, v32, 0x3baaaaab, v163
	v_mul_f32_e32 v36, 0x4b800000, v32
	v_cmp_gt_f32_e32 vcc, s69, v32
	s_nop 1
	v_cndmask_b32_e32 v32, v32, v36, vcc
	v_rsq_f32_e32 v209, v32
	v_mov_b32_e32 v32, v37
	v_mov_b32_e32 v37, v30
	v_mov_b32_e32 v36, v34
	v_mul_f32_e32 v30, 0x45800000, v209
	v_cndmask_b32_e32 v30, v209, v30, vcc
	v_mul_f32_e32 v34, 0x3dd53b94, v30
	s_waitcnt vmcnt(22)
	v_mul_f32_e32 v30, v114, v34
	v_mul_f32_e32 v114, v30, v177
	v_mul_f32_e32 v30, v110, v34
	v_mul_f32_e32 v110, v30, v180
	v_mul_f32_e32 v30, v115, v34
	v_mul_f32_e32 v115, v30, v174
	v_mul_f32_e32 v30, v111, v34
	v_mul_f32_e32 v111, v30, v176
	v_mul_f32_e32 v30, v116, v34
	v_mul_f32_e32 v116, v30, v170
	v_mul_f32_e32 v30, v112, v34
	v_mul_f32_e32 v112, v30, v171
	v_mul_f32_e32 v30, v117, v34
	v_mul_f32_e32 v117, v30, v167
	v_mul_f32_e32 v30, v113, v34
	v_mul_f32_e32 v113, v30, v169
	s_waitcnt vmcnt(20)
	v_mul_f32_e32 v30, v106, v34
	v_mul_f32_e32 v106, v30, v185
	v_mul_f32_e32 v30, v102, v34
	v_mul_f32_e32 v167, v30, v187
	v_mul_f32_e32 v30, v107, v34
	v_mul_f32_e32 v102, v30, v182
	v_mul_f32_e32 v30, v103, v34
	v_mul_f32_e32 v107, v30, v183
	v_mul_f32_e32 v30, v108, v34
	v_mul_f32_e32 v103, v30, v179
	v_mul_f32_e32 v30, v104, v34
	v_mul_f32_e32 v108, v30, v181
	v_mul_f32_e32 v30, v109, v34
	v_mul_f32_e32 v104, v30, v175
	v_mul_f32_e32 v30, v105, v34
	v_mul_f32_e32 v105, v30, v178
	s_waitcnt vmcnt(18)
	v_mul_f32_e32 v30, v98, v34
	v_mul_f32_e32 v109, v30, v193
	v_mul_f32_e32 v30, v94, v34
	v_mul_f32_e32 v94, v30, v195
	v_mul_f32_e32 v30, v99, v34
	v_mul_f32_e32 v169, v30, v190
	v_mul_f32_e32 v30, v95, v34
	v_mul_f32_e32 v95, v30, v191
	v_mul_f32_e32 v30, v100, v34
	v_mul_f32_e32 v170, v30, v188
	v_mul_f32_e32 v30, v96, v34
	v_mul_f32_e32 v96, v30, v189
	v_mul_f32_e32 v30, v101, v34
	v_mul_f32_e32 v171, v30, v184
	v_mul_f32_e32 v30, v97, v34
	v_mul_f32_e32 v97, v30, v186
	s_waitcnt vmcnt(16)
	v_mul_f32_e32 v30, v90, v34
	v_mul_f32_e32 v90, v30, v201
	v_mul_f32_e32 v30, v86, v34
	v_mul_f32_e32 v86, v30, v202
	v_mul_f32_e32 v30, v91, v34
	v_mul_f32_e32 v91, v30, v198
	v_mul_f32_e32 v30, v87, v34
	v_mul_f32_e32 v87, v30, v199
	v_mul_f32_e32 v30, v92, v34
	v_mul_f32_e32 v92, v30, v196
	v_mul_f32_e32 v30, v88, v34
	v_mul_f32_e32 v88, v30, v197
	v_mul_f32_e32 v30, v93, v34
	v_mul_f32_e32 v93, v30, v192
	v_mul_f32_e32 v30, v89, v34
	v_mul_f32_e32 v89, v30, v194
	s_waitcnt vmcnt(14)
	v_mul_f32_e32 v30, v82, v34
	v_mul_f32_e32 v82, v30, v207
	v_mul_f32_e32 v30, v34, v78
	v_mul_f32_e32 v78, v30, v208
	v_mul_f32_e32 v30, v83, v34
	v_mul_f32_e32 v83, v30, v205
	v_mul_f32_e32 v30, v34, v79
	v_mul_f32_e32 v79, v30, v206
	v_mul_f32_e32 v30, v84, v34
	v_mul_f32_e32 v84, v30, v203
	v_mul_f32_e32 v30, v34, v80
	v_mul_f32_e32 v80, v30, v204
	v_mul_f32_e32 v30, v85, v34
	v_mul_f32_e32 v85, v30, v200
	v_mul_f32_e32 v30, v34, v81
	v_mul_f32_e32 v81, v30, v226
	s_waitcnt vmcnt(12)
	v_mul_f32_e32 v30, v34, v74
	v_mul_f32_e32 v74, v30, v227
	v_mul_f32_e32 v30, v34, v70
	v_mul_f32_e32 v70, v30, v231
	v_mul_f32_e32 v30, v34, v75
	v_mul_f32_e32 v75, v30, v228
	v_mul_f32_e32 v30, v34, v71
	v_mul_f32_e32 v71, v30, v232
	v_mul_f32_e32 v30, v34, v76
	v_mul_f32_e32 v76, v30, v229
	v_mul_f32_e32 v30, v34, v72
	v_mul_f32_e32 v72, v30, v233
	v_mul_f32_e32 v30, v34, v77
	v_mul_f32_e32 v77, v30, v230
	v_mul_f32_e32 v30, v34, v73
	v_mul_f32_e32 v73, v30, v234
	s_waitcnt vmcnt(10)
	v_mul_f32_e32 v30, v34, v66
	v_mul_f32_e32 v174, v30, v235
	v_mul_f32_e32 v30, v34, v62
	v_mul_f32_e32 v175, v30, v239
	v_mul_f32_e32 v30, v34, v67
	v_mul_f32_e32 v176, v30, v236
	v_mul_f32_e32 v30, v34, v63
	v_mul_f32_e32 v177, v30, v240
	v_mul_f32_e32 v30, v34, v68
	v_mul_f32_e32 v68, v30, v237
	v_mul_f32_e32 v30, v34, v64
	v_mul_f32_e32 v178, v30, v241
	v_mul_f32_e32 v30, v34, v69
	v_mul_f32_e32 v69, v30, v238
	v_mul_f32_e32 v30, v34, v65
	v_mul_f32_e32 v179, v30, v242
	s_waitcnt vmcnt(8)
	v_mul_f32_e32 v30, v34, v58
	v_mul_f32_e32 v180, v30, v243
	v_mul_f32_e32 v30, v34, v54
	v_mul_f32_e32 v181, v30, v247
	v_mul_f32_e32 v30, v34, v59
	v_mul_f32_e32 v182, v30, v244
	v_mul_f32_e32 v30, v34, v55
	v_mul_f32_e32 v183, v30, v248
	v_mul_f32_e32 v30, v34, v60
	v_mul_f32_e32 v184, v30, v245
	v_mul_f32_e32 v30, v34, v56
	v_mul_f32_e32 v185, v30, v249
	v_mul_f32_e32 v30, v34, v61
	v_mul_f32_e32 v186, v30, v246
	v_mul_f32_e32 v30, v34, v57
	v_mul_f32_e32 v36, v34, v36
	v_mul_f32_e32 v37, v34, v37
	v_mul_f32_e32 v187, v30, v250
	v_mul_f32_e32 v36, v36, v222
	v_mul_f32_e32 v37, v37, v223
	v_mov_b32_e32 v30, v35
	v_mul_f32_e32 v54, v34, v158
	v_mul_f32_e32 v55, v34, v159
	v_mul_f32_e32 v30, v34, v30
	v_mul_f32_e32 v31, v34, v31
	v_mul_f32_e32 v26, v34, v26
	v_mul_f32_e32 v27, v34, v27
	v_mul_f32_e32 v56, v34, v212
	v_mul_f32_e32 v57, v34, v213
	v_mul_f32_e32 v58, v34, v150
	v_mul_f32_e32 v59, v34, v151
	v_mul_f32_e32 v32, v34, v32
	v_mul_f32_e32 v33, v34, v33
	v_mul_f32_e32 v28, v34, v28
	v_mul_f32_e32 v29, v34, v29
	v_mul_f32_e32 v60, v34, v140
	v_mul_f32_e32 v61, v34, v141
	v_mul_f32_e32 v62, v34, v128
	v_mul_f32_e32 v63, v34, v129
	v_mul_f32_e32 v14, v34, v14
	v_mul_f32_e32 v15, v34, v15
	v_mul_f32_e32 v6, v34, v6
	v_mul_f32_e32 v7, v34, v7
	v_mul_f32_e32 v64, v34, v134
	v_mul_f32_e32 v65, v34, v135
	v_mul_f32_e32 v66, v34, v122
	v_mul_f32_e32 v67, v34, v123
	v_mul_f32_e32 v16, v34, v16
	v_mul_f32_e32 v17, v34, v17
	v_mul_f32_e32 v8, v34, v8
	v_mul_f32_e32 v9, v34, v9
	s_waitcnt vmcnt(4)
	v_mul_f32_e32 v34, v37, v50
	v_mul_f32_e32 v35, v36, v51
	v_mul_f32_e32 v30, v30, v224
	v_mul_f32_e32 v31, v31, v225
	v_mul_f32_e32 v64, v64, v130
	v_mul_f32_e32 v65, v65, v131
	v_sub_f32_e32 v130, v34, v35
	v_mul_f32_e32 v34, v36, v50
	v_mul_f32_e32 v35, v37, v51
	v_mul_f32_e32 v56, v56, v156
	v_mul_f32_e32 v57, v57, v157
	v_add_f32_e32 v36, v35, v34
	v_mul_f32_e32 v34, v31, v52
	v_mul_f32_e32 v35, v30, v53
	v_mul_f32_e32 v30, v30, v52
	v_mul_f32_e32 v31, v31, v53
	v_sub_f32_e32 v34, v34, v35
	v_add_f32_e32 v35, v31, v30
	v_mul_f32_e32 v30, v57, v38
	v_mul_f32_e32 v31, v56, v39
	v_mul_f32_e32 v32, v32, v160
	v_mul_f32_e32 v33, v33, v161
	v_sub_f32_e32 v37, v30, v31
	v_mul_f32_e32 v30, v56, v38
	v_mul_f32_e32 v31, v57, v39
	v_mul_f32_e32 v54, v54, v152
	v_mul_f32_e32 v55, v55, v153
	v_add_f32_e32 v38, v31, v30
	v_mul_f32_e32 v30, v33, v40
	v_mul_f32_e32 v31, v32, v41
	v_sub_f32_e32 v39, v30, v31
	v_mul_f32_e32 v30, v32, v40
	v_mul_f32_e32 v31, v33, v41
	v_mul_f32_e32 v26, v26, v154
	v_mul_f32_e32 v27, v27, v155
	v_add_f32_e32 v32, v31, v30
	v_mul_f32_e32 v30, v55, v22
	v_mul_f32_e32 v31, v54, v23
	v_mul_f32_e32 v22, v54, v22
	v_mul_f32_e32 v23, v55, v23
	v_sub_f32_e32 v30, v30, v31
	v_add_f32_e32 v31, v23, v22
	v_mul_f32_e32 v22, v27, v24
	v_mul_f32_e32 v23, v26, v25
	v_mul_f32_e32 v58, v58, v142
	v_mul_f32_e32 v59, v59, v143
	v_sub_f32_e32 v33, v22, v23
	v_mul_f32_e32 v22, v26, v24
	v_mul_f32_e32 v23, v27, v25
	v_mul_f32_e32 v28, v28, v144
	v_mul_f32_e32 v29, v29, v145
	v_add_f32_e32 v24, v23, v22
	v_mul_f32_e32 v22, v59, v18
	v_mul_f32_e32 v23, v58, v19
	v_mul_f32_e32 v18, v58, v18
	v_mul_f32_e32 v19, v59, v19
	v_sub_f32_e32 v22, v22, v23
	v_add_f32_e32 v23, v19, v18
	v_mul_f32_e32 v18, v29, v20
	v_mul_f32_e32 v19, v28, v21
	v_mul_f32_e32 v60, v60, v136
	v_mul_f32_e32 v61, v61, v137
	v_sub_f32_e32 v25, v18, v19
	v_mul_f32_e32 v18, v28, v20
	v_mul_f32_e32 v19, v29, v21
	v_mul_f32_e32 v14, v14, v138
	v_mul_f32_e32 v15, v15, v139
	v_add_f32_e32 v20, v19, v18
	s_waitcnt vmcnt(0)
	v_mul_f32_e32 v18, v61, v46
	v_mul_f32_e32 v19, v60, v47
	v_sub_f32_e32 v21, v18, v19
	v_mul_f32_e32 v18, v60, v46
	v_mul_f32_e32 v19, v61, v47
	v_mul_f32_e32 v16, v16, v132
	v_mul_f32_e32 v17, v17, v133
	v_add_f32_e32 v26, v19, v18
	v_mul_f32_e32 v18, v15, v48
	v_mul_f32_e32 v19, v14, v49
	v_mul_f32_e32 v14, v14, v48
	v_mul_f32_e32 v15, v15, v49
	v_sub_f32_e32 v18, v18, v19
	v_add_f32_e32 v19, v15, v14
	v_mul_f32_e32 v14, v65, v42
	v_mul_f32_e32 v15, v64, v43
	v_sub_f32_e32 v27, v14, v15
	v_mul_f32_e32 v14, v64, v42
	v_mul_f32_e32 v15, v65, v43
	v_mul_f32_e32 v62, v62, v124
	v_mul_f32_e32 v63, v63, v125
	v_add_f32_e32 v28, v15, v14
	v_mul_f32_e32 v14, v17, v44
	v_mul_f32_e32 v15, v16, v45
	v_sub_f32_e32 v29, v14, v15
	v_mul_f32_e32 v14, v16, v44
	v_mul_f32_e32 v15, v17, v45
	v_mul_f32_e32 v6, v6, v126
	v_mul_f32_e32 v7, v7, v127
	v_add_f32_e32 v16, v15, v14
	v_mul_f32_e32 v14, v63, v10
	v_mul_f32_e32 v15, v62, v11
	v_mul_f32_e32 v10, v62, v10
	v_mul_f32_e32 v11, v63, v11
	v_mul_f32_e32 v66, v66, v118
	v_mul_f32_e32 v67, v67, v119
	v_sub_f32_e32 v14, v14, v15
	v_add_f32_e32 v15, v11, v10
	v_mul_f32_e32 v10, v7, v12
	v_mul_f32_e32 v11, v6, v13
	v_mul_f32_e32 v6, v6, v12
	v_mul_f32_e32 v7, v7, v13
	v_mul_f32_e32 v8, v8, v120
	v_mul_f32_e32 v9, v9, v121
	v_sub_f32_e32 v10, v10, v11
	v_add_f32_e32 v11, v7, v6
	v_mul_f32_e32 v6, v67, v2
	v_mul_f32_e32 v7, v66, v3
	v_mul_f32_e32 v2, v66, v2
	v_mul_f32_e32 v3, v67, v3
	v_sub_f32_e32 v6, v6, v7
	v_add_f32_e32 v7, v3, v2
	v_mul_f32_e32 v2, v9, v4
	v_mul_f32_e32 v3, v8, v5
	v_sub_f32_e32 v12, v2, v3
	v_mul_f32_e32 v2, v8, v4
	v_mul_f32_e32 v3, v9, v5
	v_cvt_pk_bf16_f32 v98, v114, v115
	v_cvt_pk_bf16_f32 v99, v116, v117
	v_cvt_pk_bf16_f32 v100, v110, v111
	v_cvt_pk_bf16_f32 v101, v112, v113
	v_cvt_pk_bf16_f32 v102, v106, v102
	s_nop 0
	v_add_f32_e32 v2, v3, v2
	v_cvt_pk_bf16_f32 v103, v103, v104
	v_cvt_pk_bf16_f32 v104, v167, v107
	v_cvt_pk_bf16_f32 v105, v108, v105
	v_cvt_pk_bf16_f32 v106, v109, v169
	v_cvt_pk_bf16_f32 v107, v170, v171
	v_cvt_pk_bf16_f32 v108, v94, v95
	v_cvt_pk_bf16_f32 v109, v96, v97
	v_cvt_pk_bf16_f32 v110, v90, v91
	v_cvt_pk_bf16_f32 v111, v92, v93
	v_cvt_pk_bf16_f32 v112, v86, v87
	v_cvt_pk_bf16_f32 v113, v88, v89
	v_cvt_pk_bf16_f32 v114, v82, v83
	v_cvt_pk_bf16_f32 v115, v84, v85
	v_cvt_pk_bf16_f32 v116, v78, v79
	v_cvt_pk_bf16_f32 v117, v80, v81
	v_cvt_pk_bf16_f32 v118, v74, v75
	v_cvt_pk_bf16_f32 v119, v76, v77
	v_cvt_pk_bf16_f32 v120, v70, v71
	v_cvt_pk_bf16_f32 v121, v72, v73
	v_cvt_pk_bf16_f32 v122, v174, v176
	v_cvt_pk_bf16_f32 v123, v68, v69
	v_cvt_pk_bf16_f32 v124, v175, v177
	v_cvt_pk_bf16_f32 v125, v178, v179
	v_cvt_pk_bf16_f32 v126, v180, v182
	v_cvt_pk_bf16_f32 v127, v184, v186
	v_cvt_pk_bf16_f32 v128, v181, v183
	v_cvt_pk_bf16_f32 v129, v185, v187
	v_cvt_pk_bf16_f32 v130, v130, v34
	v_cvt_pk_bf16_f32 v131, v37, v39
	v_cvt_pk_bf16_f32 v132, v30, v33
	v_cvt_pk_bf16_f32 v133, v22, v25
	v_cvt_pk_bf16_f32 v134, v21, v18
	v_cvt_pk_bf16_f32 v135, v27, v29
	v_cvt_pk_bf16_f32 v136, v14, v10
	v_cvt_pk_bf16_f32 v137, v6, v12
	v_cvt_pk_bf16_f32 v138, v36, v35
	v_cvt_pk_bf16_f32 v139, v38, v32
	v_cvt_pk_bf16_f32 v140, v31, v24
	v_cvt_pk_bf16_f32 v141, v23, v20
	v_cvt_pk_bf16_f32 v142, v26, v19
	v_cvt_pk_bf16_f32 v143, v28, v16
	v_cvt_pk_bf16_f32 v144, v15, v11
	v_cvt_pk_bf16_f32 v145, v7, v2
	v_mul_hi_i32 v2, v172, s70
	v_lshrrev_b32_e32 v3, 31, v2
	v_ashrrev_i32_e32 v2, 2, v2
	v_add_u32_e32 v2, v2, v3
	v_mul_lo_u32 v3, v2, 24
	v_sub_u32_e32 v3, v172, v3
	v_lshrrev_b32_e32 v16, 1, v2
	v_bitop3_b32 v3, v16, v3, 7 bitop3:0x6c
	v_mul_lo_u32 v2, v2, s68
	v_lshl_add_u32 v2, v3, 4, v2
	v_add_u32_e32 v3, 0x200, v172
	v_mul_hi_i32 v4, v3, s70
	v_lshrrev_b32_e32 v5, 31, v4
	v_ashrrev_i32_e32 v4, 2, v4
	v_add_u32_e32 v4, v4, v5
	v_mul_lo_u32 v5, v4, 24
	v_sub_u32_e32 v5, v3, v5
	v_lshrrev_b32_e32 v16, 1, v4
	v_bitop3_b32 v5, v16, v5, 7 bitop3:0x6c
	v_mul_lo_u32 v4, v4, s68
	v_lshl_add_u32 v4, v5, 4, v4
	v_add_u32_e32 v5, 0x400, v172
	v_mul_hi_i32 v6, v5, s70
	v_lshrrev_b32_e32 v7, 31, v6
	v_ashrrev_i32_e32 v6, 2, v6
	v_add_u32_e32 v6, v6, v7
	v_mul_lo_u32 v7, v6, 24
	v_sub_u32_e32 v5, v5, v7
	v_lshrrev_b32_e32 v16, 1, v6
	v_bitop3_b32 v5, v16, v5, 7 bitop3:0x6c
	v_mul_lo_u32 v6, v6, s68
	v_ashrrev_i32_e32 v9, 4, v172
	v_lshl_add_u32 v6, v5, 4, v6
	v_bfe_u32 v5, v172, 2, 2
	v_lshrrev_b32_e32 v7, 1, v172
	v_and_b32_e32 v10, 0x1ffff0, v9
	v_lshrrev_b32_e32 v9, 1, v9
	v_ashrrev_i32_e32 v3, 4, v3
	v_and_or_b32 v5, v7, 8, v5
	v_and_b32_e32 v7, 0x60, v172
	v_lshlrev_b32_e32 v8, 3, v172
	v_and_b32_e32 v9, 4, v9
	v_and_b32_e32 v11, 0x1ffff0, v3
	v_lshrrev_b32_e32 v3, 1, v3
	v_and_or_b32 v7, v8, 24, v7
	v_or3_b32 v9, v10, v9, v5
	v_and_b32_e32 v3, 4, v3
	s_barrier
	global_load_lds_dwordx4 v2, s[44:45]
	s_mov_b32 m0, s72
	v_lshlrev_b32_e32 v7, 1, v7
	v_lshlrev_b32_e32 v10, 11, v9
	v_or3_b32 v3, v11, v3, v5
	global_load_lds_dwordx4 v4, s[44:45]
	s_mov_b32 m0, s73
	v_or_b32_e32 v9, v10, v7
	v_lshlrev_b32_e32 v11, 11, v3
	global_load_lds_dwordx4 v6, s[44:45]
	s_mov_b32 m0, s64
	v_or_b32_e32 v3, v11, v7
	global_load_lds_dwordx4 v9, s[46:47]
	s_mov_b32 m0, s74
	v_lshlrev_b32_e32 v13, 1, v172
	global_load_lds_dwordx4 v3, s[46:47]
	v_lshlrev_b32_e32 v9, 4, v172
	v_and_b32_e32 v14, 32, v13
	v_or_b32_e32 v3, 32, v148
	v_and_b32_e32 v16, 0x13, v168
	v_and_b32_e32 v17, 4, v168
	v_lshl_or_b32 v16, v17, 1, v16
	v_and_b32_e32 v17, 8, v168
	v_lshrrev_b32_e32 v17, 1, v17
	v_or_b32_e32 v16, v16, v17
	v_mul_u32_u24_e32 v5, 0x180, v16
	v_lshlrev_b32_e32 v17, 3, v16
	v_and_b32_e32 v7, 0x70, v17
	v_and_b32_e32 v12, 0xc0, v9
	v_and_or_b32 v8, v8, s75, v14
	v_and_b32_e32 v167, 63, v172
	v_bitop3_b32 v169, v3, v5, v7 bitop3:0xde
	v_or_b32_e32 v3, 64, v148
	v_add3_u32 v172, v12, 0, v8
	v_and_b32_e32 v12, 0xc0, v13
	v_and_b32_e32 v13, 48, v9
	v_bitop3_b32 v170, v3, v5, v7 bitop3:0xde
	v_or_b32_e32 v3, 0x60, v148
	v_or3_b32 v8, v11, v12, v13
	v_mov_b32_e32 v9, v149
	v_bitop3_b32 v161, v148, v5, v7 bitop3:0xde
	v_bitop3_b32 v171, v3, v5, v7 bitop3:0xde
	v_mov_b32_e32 v3, v149
	v_mov_b32_e32 v5, v149
	v_mov_b32_e32 v7, v149
	v_mul_i32_i24_e32 v15, -8, v173
	v_lshl_add_u64 v[150:151], s[48:49], 0, v[8:9]
	v_mov_b32_e32 v240, v8
	v_or3_b32 v8, v10, v12, v13
	v_mov_b32_e32 v16, v149
	v_mov_b32_e32 v17, v149
	v_lshl_add_u32 v160, v168, 2, s65
	v_lshl_add_u64 v[152:153], s[48:49], 0, v[8:9]
	v_mov_b32_e32 v241, v8
	v_lshl_add_u64 v[154:155], s[50:51], 0, v[6:7]
	v_mov_b32_e32 v242, v6
	v_lshl_add_u64 v[156:157], s[50:51], 0, v[4:5]
	v_mov_b32_e32 v243, v4
	v_lshl_add_u64 v[158:159], s[50:51], 0, v[2:3]
	v_mov_b32_e32 v244, v2
	s_add_u32 s94, s2, s50
	s_addc_u32 s95, s3, s51
	s_add_u32 s96, s2, s48
	s_addc_u32 s97, s3, s49
	v_add3_u32 v168, s63, v15, v168
	v_mov_b32_e32 v2, v149
	v_mov_b32_e32 v4, v149
	v_mov_b32_e32 v6, v149
	v_mov_b32_e32 v8, v149
	v_mov_b32_e32 v10, v149
	v_mov_b32_e32 v11, v149
	v_mov_b32_e32 v12, v149
	v_mov_b32_e32 v13, v149
	v_mov_b32_e32 v14, v149
	v_mov_b32_e32 v15, v149
	v_mov_b64_e32 v[32:33], v[16:17]
	v_mov_b64_e32 v[48:49], v[16:17]
	v_mov_b64_e32 v[64:65], v[16:17]
	v_cmp_gt_u32_e64 s[0:1], 32, v167
	v_mov_b32_e32 v173, 0
	v_mov_b32_e32 v206, 0
	v_mov_b32_e32 v207, 0
	v_mov_b32_e32 v208, 0
	v_mov_b32_e32 v209, 0
	v_mov_b32_e32 v210, 0
	v_mov_b32_e32 v211, 0
	v_mov_b32_e32 v212, 0
	v_mov_b32_e32 v213, 0
	v_mov_b32_e32 v214, 0
	v_mov_b32_e32 v215, 0
	v_mov_b32_e32 v216, 0
	v_mov_b32_e32 v217, 0
	v_mov_b32_e32 v218, 0
	v_mov_b32_e32 v219, 0
	v_mov_b32_e32 v220, 0
	v_mov_b32_e32 v221, 0
	v_mov_b64_e32 v[30:31], v[14:15]
	v_mov_b64_e32 v[28:29], v[12:13]
	v_mov_b64_e32 v[26:27], v[10:11]
	v_mov_b64_e32 v[24:25], v[8:9]
	v_mov_b64_e32 v[22:23], v[6:7]
	v_mov_b64_e32 v[20:21], v[4:5]
	v_mov_b64_e32 v[18:19], v[2:3]
	v_mov_b64_e32 v[46:47], v[14:15]
	v_mov_b64_e32 v[44:45], v[12:13]
	v_mov_b64_e32 v[42:43], v[10:11]
	v_mov_b64_e32 v[40:41], v[8:9]
	v_mov_b64_e32 v[38:39], v[6:7]
	v_mov_b64_e32 v[36:37], v[4:5]
	v_mov_b64_e32 v[34:35], v[2:3]
	v_mov_b64_e32 v[62:63], v[14:15]
	v_mov_b64_e32 v[60:61], v[12:13]
	v_mov_b64_e32 v[58:59], v[10:11]
	v_mov_b64_e32 v[56:57], v[8:9]
	v_mov_b64_e32 v[54:55], v[6:7]
	v_mov_b64_e32 v[52:53], v[4:5]
	v_mov_b64_e32 v[50:51], v[2:3]
	v_mov_b32_e32 v174, 0
	s_cmp_ge_u32 s64, 0x1000
	s_cbranch_scc0 .Lprio_skip_a1
	s_setprio 1
.Lprio_skip_a1:
.LBB0_805:
	s_add_i32 s56, s12, -1
	s_waitcnt vmcnt(0)
	s_and_b32 s87, s56, 1
	s_cmp_ge_u32 s12, s85
	s_waitcnt vmcnt(0) lgkmcnt(0)
	s_barrier
	s_cbranch_scc1 .LBB0_807
	s_xor_b32 s56, s87, 1
	s_mulk_i32 s56, 0x6000
	s_add_i32 s56, s64, s56
	s_add_i32 m0, s56, 0x8000
	s_nop 0
	global_load_lds_dwordx4 v244, s[94:95]
	s_add_i32 m0, s56, 0xa000
	s_nop 0
	global_load_lds_dwordx4 v243, s[94:95]
	s_add_i32 m0, s56, 0xc000
	s_lshl_b32 s56, s87, 14
	s_xor_b32 s56, s56, 0x4000
	s_add_i32 s56, s64, s56
	global_load_lds_dwordx4 v242, s[94:95]
	s_mov_b32 m0, s56
	s_nop 0
	global_load_lds_dwordx4 v241, s[96:97]
	s_add_i32 m0, s56, 0x2000
	s_nop 0
	global_load_lds_dwordx4 v240, s[96:97]



.LBB0_817:
	s_or_b64 exec, exec, s[56:57]
	s_waitcnt lgkmcnt(0)
	s_lshl_b64 s[0:1], s[54:55], 11
	s_add_u32 s0, s61, s0
	s_addc_u32 s1, s62, s1
	s_add_u32 s0, s0, s79
	s_addc_u32 s1, s1, 0
	s_mov_b32 s56, 0x05040100
	v_and_b32_e32 v85, 3, v164
	v_lshl_add_u32 v83, v85, 8, v85
	v_add_u32_e32 v83, 0x0c0c0400, v83
	v_lshrrev_b32_e32 v87, 5, v164
	v_lshl_add_u32 v84, v87, 2, v85
	v_lshlrev_b32_e32 v84, 11, v84
	v_and_b32_e32 v85, 28, v164
	v_add_u32_e32 v84, v84, v85
	v_lshl_add_u32 v87, v87, 4, s65
	ds_read_b128 v[66:69], v87 offset:128
	v_mov_b32_e32 v86, v84
	s_waitcnt lgkmcnt(0)
	v_mul_f32_e32 v66, 0x41800000, v66
	v_mul_f32_e32 v67, 0x41800000, v67
	v_mul_f32_e32 v68, 0x41800000, v68
	v_mul_f32_e32 v69, 0x41800000, v69
	v_mul_f32_e32 v70, v50, v66
	v_mul_f32_e32 v71, v51, v67
	v_mul_f32_e32 v72, v52, v68
	v_mul_f32_e32 v73, v53, v69
	v_med3_f32 v70, v70, s77, v166
	v_med3_f32 v71, v71, s77, v166
	v_med3_f32 v72, v72, s77, v166
	v_med3_f32 v73, v73, s77, v166
	v_cvt_pk_fp8_f32 v74, v70, v71
	v_cvt_pk_fp8_f32 v74, v72, v73 op_sel:[0,0,1]
	s_nop 1
	v_mov_b32_dpp v75, v74 quad_perm:[0,0,0,0] row_mask:0xf bank_mask:0xf
	v_mov_b32_dpp v76, v74 quad_perm:[1,1,1,1] row_mask:0xf bank_mask:0xf
	v_mov_b32_dpp v77, v74 quad_perm:[2,2,2,2] row_mask:0xf bank_mask:0xf
	v_mov_b32_dpp v78, v74 quad_perm:[3,3,3,3] row_mask:0xf bank_mask:0xf
	v_perm_b32 v80, v76, v75, v83
	v_perm_b32 v81, v78, v77, v83
	v_perm_b32 v82, v81, v80, s56
	global_store_dword v86, v82, s[0:1]
	v_mul_f32_e32 v70, v34, v66
	v_mul_f32_e32 v71, v35, v67
	v_mul_f32_e32 v72, v36, v68
	v_mul_f32_e32 v73, v37, v69
	v_med3_f32 v70, v70, s77, v166
	v_med3_f32 v71, v71, s77, v166
	v_med3_f32 v72, v72, s77, v166
	v_med3_f32 v73, v73, s77, v166
	v_cvt_pk_fp8_f32 v74, v70, v71
	v_cvt_pk_fp8_f32 v74, v72, v73 op_sel:[0,0,1]
	s_nop 1
	v_mov_b32_dpp v75, v74 quad_perm:[0,0,0,0] row_mask:0xf bank_mask:0xf
	v_mov_b32_dpp v76, v74 quad_perm:[1,1,1,1] row_mask:0xf bank_mask:0xf
	v_mov_b32_dpp v77, v74 quad_perm:[2,2,2,2] row_mask:0xf bank_mask:0xf
	v_mov_b32_dpp v78, v74 quad_perm:[3,3,3,3] row_mask:0xf bank_mask:0xf
	v_perm_b32 v80, v76, v75, v83
	v_perm_b32 v81, v78, v77, v83
	v_perm_b32 v82, v81, v80, s56
	global_store_dword v86, v82, s[0:1] offset:32
	v_mul_f32_e32 v70, v18, v66
	v_mul_f32_e32 v71, v19, v67
	v_mul_f32_e32 v72, v20, v68
	v_mul_f32_e32 v73, v21, v69
	v_med3_f32 v70, v70, s77, v166
	v_med3_f32 v71, v71, s77, v166
	v_med3_f32 v72, v72, s77, v166
	v_med3_f32 v73, v73, s77, v166
	v_cvt_pk_fp8_f32 v74, v70, v71
	v_cvt_pk_fp8_f32 v74, v72, v73 op_sel:[0,0,1]
	s_nop 1
	v_mov_b32_dpp v75, v74 quad_perm:[0,0,0,0] row_mask:0xf bank_mask:0xf
	v_mov_b32_dpp v76, v74 quad_perm:[1,1,1,1] row_mask:0xf bank_mask:0xf
	v_mov_b32_dpp v77, v74 quad_perm:[2,2,2,2] row_mask:0xf bank_mask:0xf
	v_mov_b32_dpp v78, v74 quad_perm:[3,3,3,3] row_mask:0xf bank_mask:0xf
	v_perm_b32 v80, v76, v75, v83
	v_perm_b32 v81, v78, v77, v83
	v_perm_b32 v82, v81, v80, s56
	global_store_dword v86, v82, s[0:1] offset:64
	v_mul_f32_e32 v70, v2, v66
	v_mul_f32_e32 v71, v3, v67
	v_mul_f32_e32 v72, v4, v68
	v_mul_f32_e32 v73, v5, v69
	v_med3_f32 v70, v70, s77, v166
	v_med3_f32 v71, v71, s77, v166
	v_med3_f32 v72, v72, s77, v166
	v_med3_f32 v73, v73, s77, v166
	v_cvt_pk_fp8_f32 v74, v70, v71
	v_cvt_pk_fp8_f32 v74, v72, v73 op_sel:[0,0,1]
	s_nop 1
	v_mov_b32_dpp v75, v74 quad_perm:[0,0,0,0] row_mask:0xf bank_mask:0xf
	v_mov_b32_dpp v76, v74 quad_perm:[1,1,1,1] row_mask:0xf bank_mask:0xf
	v_mov_b32_dpp v77, v74 quad_perm:[2,2,2,2] row_mask:0xf bank_mask:0xf
	v_mov_b32_dpp v78, v74 quad_perm:[3,3,3,3] row_mask:0xf bank_mask:0xf
	v_perm_b32 v80, v76, v75, v83
	v_perm_b32 v81, v78, v77, v83
	v_perm_b32 v82, v81, v80, s56
	global_store_dword v86, v82, s[0:1] offset:96
	ds_read_b128 v[66:69], v87 offset:160
	v_add_u32_e32 v86, 0x4000, v84
	s_waitcnt lgkmcnt(0)
	v_mul_f32_e32 v66, 0x41800000, v66
	v_mul_f32_e32 v67, 0x41800000, v67
	v_mul_f32_e32 v68, 0x41800000, v68
	v_mul_f32_e32 v69, 0x41800000, v69
	v_mul_f32_e32 v70, v54, v66
	v_mul_f32_e32 v71, v55, v67
	v_mul_f32_e32 v72, v56, v68
	v_mul_f32_e32 v73, v57, v69
	v_med3_f32 v70, v70, s77, v166
	v_med3_f32 v71, v71, s77, v166
	v_med3_f32 v72, v72, s77, v166
	v_med3_f32 v73, v73, s77, v166
	v_cvt_pk_fp8_f32 v74, v70, v71
	v_cvt_pk_fp8_f32 v74, v72, v73 op_sel:[0,0,1]
	s_nop 1
	v_mov_b32_dpp v75, v74 quad_perm:[0,0,0,0] row_mask:0xf bank_mask:0xf
	v_mov_b32_dpp v76, v74 quad_perm:[1,1,1,1] row_mask:0xf bank_mask:0xf
	v_mov_b32_dpp v77, v74 quad_perm:[2,2,2,2] row_mask:0xf bank_mask:0xf
	v_mov_b32_dpp v78, v74 quad_perm:[3,3,3,3] row_mask:0xf bank_mask:0xf
	v_perm_b32 v80, v76, v75, v83
	v_perm_b32 v81, v78, v77, v83
	v_perm_b32 v82, v81, v80, s56
	global_store_dword v86, v82, s[0:1]
	v_mul_f32_e32 v70, v38, v66
	v_mul_f32_e32 v71, v39, v67
	v_mul_f32_e32 v72, v40, v68
	v_mul_f32_e32 v73, v41, v69
	v_med3_f32 v70, v70, s77, v166
	v_med3_f32 v71, v71, s77, v166
	v_med3_f32 v72, v72, s77, v166
	v_med3_f32 v73, v73, s77, v166
	v_cvt_pk_fp8_f32 v74, v70, v71
	v_cvt_pk_fp8_f32 v74, v72, v73 op_sel:[0,0,1]
	s_nop 1
	v_mov_b32_dpp v75, v74 quad_perm:[0,0,0,0] row_mask:0xf bank_mask:0xf
	v_mov_b32_dpp v76, v74 quad_perm:[1,1,1,1] row_mask:0xf bank_mask:0xf
	v_mov_b32_dpp v77, v74 quad_perm:[2,2,2,2] row_mask:0xf bank_mask:0xf
	v_mov_b32_dpp v78, v74 quad_perm:[3,3,3,3] row_mask:0xf bank_mask:0xf
	v_perm_b32 v80, v76, v75, v83
	v_perm_b32 v81, v78, v77, v83
	v_perm_b32 v82, v81, v80, s56
	global_store_dword v86, v82, s[0:1] offset:32
	v_mul_f32_e32 v70, v22, v66
	v_mul_f32_e32 v71, v23, v67
	v_mul_f32_e32 v72, v24, v68
	v_mul_f32_e32 v73, v25, v69
	v_med3_f32 v70, v70, s77, v166
	v_med3_f32 v71, v71, s77, v166
	v_med3_f32 v72, v72, s77, v166
	v_med3_f32 v73, v73, s77, v166
	v_cvt_pk_fp8_f32 v74, v70, v71
	v_cvt_pk_fp8_f32 v74, v72, v73 op_sel:[0,0,1]
	s_nop 1
	v_mov_b32_dpp v75, v74 quad_perm:[0,0,0,0] row_mask:0xf bank_mask:0xf
	v_mov_b32_dpp v76, v74 quad_perm:[1,1,1,1] row_mask:0xf bank_mask:0xf
	v_mov_b32_dpp v77, v74 quad_perm:[2,2,2,2] row_mask:0xf bank_mask:0xf
	v_mov_b32_dpp v78, v74 quad_perm:[3,3,3,3] row_mask:0xf bank_mask:0xf
	v_perm_b32 v80, v76, v75, v83
	v_perm_b32 v81, v78, v77, v83
	v_perm_b32 v82, v81, v80, s56
	global_store_dword v86, v82, s[0:1] offset:64
	v_mul_f32_e32 v70, v6, v66
	v_mul_f32_e32 v71, v7, v67
	v_mul_f32_e32 v72, v8, v68
	v_mul_f32_e32 v73, v9, v69
	v_med3_f32 v70, v70, s77, v166
	v_med3_f32 v71, v71, s77, v166
	v_med3_f32 v72, v72, s77, v166
	v_med3_f32 v73, v73, s77, v166
	v_cvt_pk_fp8_f32 v74, v70, v71
	v_cvt_pk_fp8_f32 v74, v72, v73 op_sel:[0,0,1]
	s_nop 1
	v_mov_b32_dpp v75, v74 quad_perm:[0,0,0,0] row_mask:0xf bank_mask:0xf
	v_mov_b32_dpp v76, v74 quad_perm:[1,1,1,1] row_mask:0xf bank_mask:0xf
	v_mov_b32_dpp v77, v74 quad_perm:[2,2,2,2] row_mask:0xf bank_mask:0xf
	v_mov_b32_dpp v78, v74 quad_perm:[3,3,3,3] row_mask:0xf bank_mask:0xf
	v_perm_b32 v80, v76, v75, v83
	v_perm_b32 v81, v78, v77, v83
	v_perm_b32 v82, v81, v80, s56
	global_store_dword v86, v82, s[0:1] offset:96
	ds_read_b128 v[66:69], v87 offset:192
	v_add_u32_e32 v86, 0x8000, v84
	s_waitcnt lgkmcnt(0)
	v_mul_f32_e32 v66, 0x41800000, v66
	v_mul_f32_e32 v67, 0x41800000, v67
	v_mul_f32_e32 v68, 0x41800000, v68
	v_mul_f32_e32 v69, 0x41800000, v69
	v_mul_f32_e32 v70, v58, v66
	v_mul_f32_e32 v71, v59, v67
	v_mul_f32_e32 v72, v60, v68
	v_mul_f32_e32 v73, v61, v69
	v_med3_f32 v70, v70, s77, v166
	v_med3_f32 v71, v71, s77, v166
	v_med3_f32 v72, v72, s77, v166
	v_med3_f32 v73, v73, s77, v166
	v_cvt_pk_fp8_f32 v74, v70, v71
	v_cvt_pk_fp8_f32 v74, v72, v73 op_sel:[0,0,1]
	s_nop 1
	v_mov_b32_dpp v75, v74 quad_perm:[0,0,0,0] row_mask:0xf bank_mask:0xf
	v_mov_b32_dpp v76, v74 quad_perm:[1,1,1,1] row_mask:0xf bank_mask:0xf
	v_mov_b32_dpp v77, v74 quad_perm:[2,2,2,2] row_mask:0xf bank_mask:0xf
	v_mov_b32_dpp v78, v74 quad_perm:[3,3,3,3] row_mask:0xf bank_mask:0xf
	v_perm_b32 v80, v76, v75, v83
	v_perm_b32 v81, v78, v77, v83
	v_perm_b32 v82, v81, v80, s56
	global_store_dword v86, v82, s[0:1]
	v_mul_f32_e32 v70, v42, v66
	v_mul_f32_e32 v71, v43, v67
	v_mul_f32_e32 v72, v44, v68
	v_mul_f32_e32 v73, v45, v69
	v_med3_f32 v70, v70, s77, v166
	v_med3_f32 v71, v71, s77, v166
	v_med3_f32 v72, v72, s77, v166
	v_med3_f32 v73, v73, s77, v166
	v_cvt_pk_fp8_f32 v74, v70, v71
	v_cvt_pk_fp8_f32 v74, v72, v73 op_sel:[0,0,1]
	s_nop 1
	v_mov_b32_dpp v75, v74 quad_perm:[0,0,0,0] row_mask:0xf bank_mask:0xf
	v_mov_b32_dpp v76, v74 quad_perm:[1,1,1,1] row_mask:0xf bank_mask:0xf
	v_mov_b32_dpp v77, v74 quad_perm:[2,2,2,2] row_mask:0xf bank_mask:0xf
	v_mov_b32_dpp v78, v74 quad_perm:[3,3,3,3] row_mask:0xf bank_mask:0xf
	v_perm_b32 v80, v76, v75, v83
	v_perm_b32 v81, v78, v77, v83
	v_perm_b32 v82, v81, v80, s56
	global_store_dword v86, v82, s[0:1] offset:32
	v_mul_f32_e32 v70, v26, v66
	v_mul_f32_e32 v71, v27, v67
	v_mul_f32_e32 v72, v28, v68
	v_mul_f32_e32 v73, v29, v69
	v_med3_f32 v70, v70, s77, v166
	v_med3_f32 v71, v71, s77, v166
	v_med3_f32 v72, v72, s77, v166
	v_med3_f32 v73, v73, s77, v166
	v_cvt_pk_fp8_f32 v74, v70, v71
	v_cvt_pk_fp8_f32 v74, v72, v73 op_sel:[0,0,1]
	s_nop 1
	v_mov_b32_dpp v75, v74 quad_perm:[0,0,0,0] row_mask:0xf bank_mask:0xf
	v_mov_b32_dpp v76, v74 quad_perm:[1,1,1,1] row_mask:0xf bank_mask:0xf
	v_mov_b32_dpp v77, v74 quad_perm:[2,2,2,2] row_mask:0xf bank_mask:0xf
	v_mov_b32_dpp v78, v74 quad_perm:[3,3,3,3] row_mask:0xf bank_mask:0xf
	v_perm_b32 v80, v76, v75, v83
	v_perm_b32 v81, v78, v77, v83
	v_perm_b32 v82, v81, v80, s56
	global_store_dword v86, v82, s[0:1] offset:64
	v_mul_f32_e32 v70, v10, v66
	v_mul_f32_e32 v71, v11, v67
	v_mul_f32_e32 v72, v12, v68
	v_mul_f32_e32 v73, v13, v69
	v_med3_f32 v70, v70, s77, v166
	v_med3_f32 v71, v71, s77, v166
	v_med3_f32 v72, v72, s77, v166
	v_med3_f32 v73, v73, s77, v166
	v_cvt_pk_fp8_f32 v74, v70, v71
	v_cvt_pk_fp8_f32 v74, v72, v73 op_sel:[0,0,1]
	s_nop 1
	v_mov_b32_dpp v75, v74 quad_perm:[0,0,0,0] row_mask:0xf bank_mask:0xf
	v_mov_b32_dpp v76, v74 quad_perm:[1,1,1,1] row_mask:0xf bank_mask:0xf
	v_mov_b32_dpp v77, v74 quad_perm:[2,2,2,2] row_mask:0xf bank_mask:0xf
	v_mov_b32_dpp v78, v74 quad_perm:[3,3,3,3] row_mask:0xf bank_mask:0xf
	v_perm_b32 v80, v76, v75, v83
	v_perm_b32 v81, v78, v77, v83
	v_perm_b32 v82, v81, v80, s56
	global_store_dword v86, v82, s[0:1] offset:96
	ds_read_b128 v[66:69], v87 offset:224
	v_add_u32_e32 v86, 0xc000, v84
	s_waitcnt lgkmcnt(0)
	v_mul_f32_e32 v66, 0x41800000, v66
	v_mul_f32_e32 v67, 0x41800000, v67
	v_mul_f32_e32 v68, 0x41800000, v68
	v_mul_f32_e32 v69, 0x41800000, v69
	v_mul_f32_e32 v70, v62, v66
	v_mul_f32_e32 v71, v63, v67
	v_mul_f32_e32 v72, v64, v68
	v_mul_f32_e32 v73, v65, v69
	v_med3_f32 v70, v70, s77, v166
	v_med3_f32 v71, v71, s77, v166
	v_med3_f32 v72, v72, s77, v166
	v_med3_f32 v73, v73, s77, v166
	v_cvt_pk_fp8_f32 v74, v70, v71
	v_cvt_pk_fp8_f32 v74, v72, v73 op_sel:[0,0,1]
	s_nop 1
	v_mov_b32_dpp v75, v74 quad_perm:[0,0,0,0] row_mask:0xf bank_mask:0xf
	v_mov_b32_dpp v76, v74 quad_perm:[1,1,1,1] row_mask:0xf bank_mask:0xf
	v_mov_b32_dpp v77, v74 quad_perm:[2,2,2,2] row_mask:0xf bank_mask:0xf
	v_mov_b32_dpp v78, v74 quad_perm:[3,3,3,3] row_mask:0xf bank_mask:0xf
	v_perm_b32 v80, v76, v75, v83
	v_perm_b32 v81, v78, v77, v83
	v_perm_b32 v82, v81, v80, s56
	global_store_dword v86, v82, s[0:1]
	v_mul_f32_e32 v70, v46, v66
	v_mul_f32_e32 v71, v47, v67
	v_mul_f32_e32 v72, v48, v68
	v_mul_f32_e32 v73, v49, v69
	v_med3_f32 v70, v70, s77, v166
	v_med3_f32 v71, v71, s77, v166
	v_med3_f32 v72, v72, s77, v166
	v_med3_f32 v73, v73, s77, v166
	v_cvt_pk_fp8_f32 v74, v70, v71
	v_cvt_pk_fp8_f32 v74, v72, v73 op_sel:[0,0,1]
	s_nop 1
	v_mov_b32_dpp v75, v74 quad_perm:[0,0,0,0] row_mask:0xf bank_mask:0xf
	v_mov_b32_dpp v76, v74 quad_perm:[1,1,1,1] row_mask:0xf bank_mask:0xf
	v_mov_b32_dpp v77, v74 quad_perm:[2,2,2,2] row_mask:0xf bank_mask:0xf
	v_mov_b32_dpp v78, v74 quad_perm:[3,3,3,3] row_mask:0xf bank_mask:0xf
	v_perm_b32 v80, v76, v75, v83
	v_perm_b32 v81, v78, v77, v83
	v_perm_b32 v82, v81, v80, s56
	global_store_dword v86, v82, s[0:1] offset:32
	v_mul_f32_e32 v70, v30, v66
	v_mul_f32_e32 v71, v31, v67
	v_mul_f32_e32 v72, v32, v68
	v_mul_f32_e32 v73, v33, v69
	v_med3_f32 v70, v70, s77, v166
	v_med3_f32 v71, v71, s77, v166
	v_med3_f32 v72, v72, s77, v166
	v_med3_f32 v73, v73, s77, v166
	v_cvt_pk_fp8_f32 v74, v70, v71
	v_cvt_pk_fp8_f32 v74, v72, v73 op_sel:[0,0,1]
	s_nop 1
	v_mov_b32_dpp v75, v74 quad_perm:[0,0,0,0] row_mask:0xf bank_mask:0xf
	v_mov_b32_dpp v76, v74 quad_perm:[1,1,1,1] row_mask:0xf bank_mask:0xf
	v_mov_b32_dpp v77, v74 quad_perm:[2,2,2,2] row_mask:0xf bank_mask:0xf
	v_mov_b32_dpp v78, v74 quad_perm:[3,3,3,3] row_mask:0xf bank_mask:0xf
	v_perm_b32 v80, v76, v75, v83
	v_perm_b32 v81, v78, v77, v83
	v_perm_b32 v82, v81, v80, s56
	global_store_dword v86, v82, s[0:1] offset:64
	v_mul_f32_e32 v70, v14, v66
	v_mul_f32_e32 v71, v15, v67
	v_mul_f32_e32 v72, v16, v68
	v_mul_f32_e32 v73, v17, v69
	v_med3_f32 v70, v70, s77, v166
	v_med3_f32 v71, v71, s77, v166
	v_med3_f32 v72, v72, s77, v166
	v_med3_f32 v73, v73, s77, v166
	v_cvt_pk_fp8_f32 v74, v70, v71
	v_cvt_pk_fp8_f32 v74, v72, v73 op_sel:[0,0,1]
	s_nop 1
	v_mov_b32_dpp v75, v74 quad_perm:[0,0,0,0] row_mask:0xf bank_mask:0xf
	v_mov_b32_dpp v76, v74 quad_perm:[1,1,1,1] row_mask:0xf bank_mask:0xf
	v_mov_b32_dpp v77, v74 quad_perm:[2,2,2,2] row_mask:0xf bank_mask:0xf
	v_mov_b32_dpp v78, v74 quad_perm:[3,3,3,3] row_mask:0xf bank_mask:0xf
	v_perm_b32 v80, v76, v75, v83
	v_perm_b32 v81, v78, v77, v83
	v_perm_b32 v82, v81, v80, s56
	global_store_dword v86, v82, s[0:1] offset:96


	s_lshl_b32 s55, s80, 8
	s_and_b32 s0, s81, 15
	s_add_i32 s55, s55, s63
	s_lshl_b32 s54, s0, 8
	v_mov_b32_e32 v168, v1
	s_ashr_i32 s0, s55, 31
	s_add_u32 s52, s52, s55
	v_and_b32_e32 v167, 31, v168
	v_or_b32_e32 v30, s52, v167
	v_mov_b64_e32 v[2:3], s[6:7]
	s_addc_u32 s53, s53, s0
	v_mad_u64_u32 v[2:3], s[0:1], v30, s68, v[2:3]
	v_bfe_u32 v169, v168, 5, 1
	v_mad_i32_i24 v3, s53, v162, v3
	s_lshl_b32 s12, s82, 1
	v_lshl_add_u64 v[2:3], v[2:3], 0, s[12:13]
	v_lshlrev_b32_e32 v148, 4, v169
	v_lshl_add_u64 v[44:45], v[2:3], 0, v[148:149]
	global_load_dwordx4 v[32:35], v[44:45], off
	global_load_dwordx4 v[36:39], v[44:45], off offset:32
	global_load_dwordx4 v[26:29], v[44:45], off offset:64
	global_load_dwordx4 v[22:25], v[44:45], off offset:96
	global_load_dwordx4 v[18:21], v[44:45], off offset:128
	global_load_dwordx4 v[14:17], v[44:45], off offset:160
	global_load_dwordx4 v[10:13], v[44:45], off offset:192
	v_and_b32_e32 v118, 32, v168
	global_load_dwordx4 v[6:9], v118, s[4:5] offset:576
	s_waitcnt lgkmcnt(0)
	global_load_dwordx4 v[2:5], v118, s[4:5] offset:592
	global_load_dwordx4 v[102:105], v118, s[4:5] offset:704
	global_load_dwordx4 v[110:113], v118, s[4:5] offset:720
	global_load_dwordx4 v[40:43], v[44:45], off offset:224
	global_load_dwordx4 v[82:85], v[44:45], off offset:256
	global_load_dwordx4 v[138:141], v[44:45], off offset:288
	global_load_dwordx4 v[70:73], v[44:45], off offset:320
	global_load_dwordx4 v[142:145], v[44:45], off offset:352
	v_mov_b32_e32 v31, s53
	s_mov_b32 m0, s71
	s_mov_b32 s12, 1
	s_waitcnt vmcnt(0)
	v_and_b32_e32 v191, 0xffff0000, v32
	v_lshlrev_b32_e32 v190, 16, v32
	v_lshlrev_b32_e32 v206, 16, v26
	v_and_b32_e32 v207, 0xffff0000, v26
	v_lshlrev_b32_e32 v208, 16, v27
	v_and_b32_e32 v209, 0xffff0000, v27
	v_lshlrev_b32_e32 v210, 16, v28
	v_and_b32_e32 v211, 0xffff0000, v28
	v_lshlrev_b32_e32 v212, 16, v29
	v_and_b32_e32 v213, 0xffff0000, v29
	v_lshlrev_b32_e32 v222, 16, v18
	v_and_b32_e32 v223, 0xffff0000, v18
	v_lshlrev_b32_e32 v224, 16, v19
	v_and_b32_e32 v225, 0xffff0000, v19
	v_lshlrev_b32_e32 v226, 16, v20
	v_and_b32_e32 v227, 0xffff0000, v20
	v_lshlrev_b32_e32 v228, 16, v21
	v_and_b32_e32 v229, 0xffff0000, v21
	global_load_dwordx4 v[26:29], v118, s[4:5] offset:640
	global_load_dwordx4 v[156:159], v118, s[4:5] offset:656
	global_load_dwordx4 v[18:21], v118, s[4:5] offset:528
	v_mul_f32_e32 v188, v191, v191
	v_lshlrev_b32_e32 v192, 16, v33
	v_fmac_f32_e32 v188, v190, v190
	v_and_b32_e32 v193, 0xffff0000, v33
	v_fmac_f32_e32 v188, v192, v192
	v_lshlrev_b32_e32 v194, 16, v34
	v_fmac_f32_e32 v188, v193, v193
	v_and_b32_e32 v195, 0xffff0000, v34
	v_fmac_f32_e32 v188, v194, v194
	v_lshlrev_b32_e32 v196, 16, v35
	v_fmac_f32_e32 v188, v195, v195
	v_and_b32_e32 v197, 0xffff0000, v35
	v_fmac_f32_e32 v188, v196, v196
	v_lshlrev_b32_e32 v198, 16, v36
	v_fmac_f32_e32 v188, v197, v197
	v_and_b32_e32 v199, 0xffff0000, v36
	v_fmac_f32_e32 v188, v198, v198
	v_lshlrev_b32_e32 v200, 16, v37
	v_lshlrev_b32_e32 v214, 16, v22
	v_and_b32_e32 v215, 0xffff0000, v22
	v_lshlrev_b32_e32 v216, 16, v23
	v_and_b32_e32 v217, 0xffff0000, v23
	v_lshlrev_b32_e32 v218, 16, v24
	v_and_b32_e32 v219, 0xffff0000, v24
	v_lshlrev_b32_e32 v220, 16, v25
	v_and_b32_e32 v221, 0xffff0000, v25
	v_fmac_f32_e32 v188, v199, v199
	global_load_dwordx4 v[22:25], v118, s[4:5] offset:512
	v_and_b32_e32 v201, 0xffff0000, v37
	v_fmac_f32_e32 v188, v200, v200
	v_lshlrev_b32_e32 v202, 16, v38
	v_fmac_f32_e32 v188, v201, v201
	v_and_b32_e32 v203, 0xffff0000, v38
	v_fmac_f32_e32 v188, v202, v202
	v_lshlrev_b32_e32 v204, 16, v39
	v_fmac_f32_e32 v188, v203, v203
	v_and_b32_e32 v205, 0xffff0000, v39
	v_fmac_f32_e32 v188, v204, v204
	v_fmac_f32_e32 v188, v205, v205
	v_fmac_f32_e32 v188, v206, v206
	v_fmac_f32_e32 v188, v207, v207
	v_fmac_f32_e32 v188, v208, v208
	v_fmac_f32_e32 v188, v209, v209
	v_fmac_f32_e32 v188, v210, v210
	v_fmac_f32_e32 v188, v211, v211
	v_fmac_f32_e32 v188, v212, v212
	v_fmac_f32_e32 v188, v213, v213
	v_fmac_f32_e32 v188, v214, v214
	v_fmac_f32_e32 v188, v215, v215
	v_fmac_f32_e32 v188, v216, v216
	v_fmac_f32_e32 v188, v217, v217
	v_fmac_f32_e32 v188, v218, v218
	v_fmac_f32_e32 v188, v219, v219
	v_fmac_f32_e32 v188, v220, v220
	v_fmac_f32_e32 v188, v221, v221
	v_fmac_f32_e32 v188, v222, v222
	v_fmac_f32_e32 v188, v223, v223
	v_fmac_f32_e32 v188, v224, v224
	v_fmac_f32_e32 v188, v225, v225
	v_fmac_f32_e32 v188, v226, v226
	v_fmac_f32_e32 v188, v227, v227
	v_fmac_f32_e32 v188, v228, v228
	v_lshlrev_b32_e32 v230, 16, v14
	v_fmac_f32_e32 v188, v229, v229
	v_and_b32_e32 v231, 0xffff0000, v14
	v_fmac_f32_e32 v188, v230, v230
	v_lshlrev_b32_e32 v232, 16, v15
	v_fmac_f32_e32 v188, v231, v231
	v_and_b32_e32 v233, 0xffff0000, v15
	v_fmac_f32_e32 v188, v232, v232
	v_lshlrev_b32_e32 v234, 16, v16
	v_fmac_f32_e32 v188, v233, v233
	v_and_b32_e32 v235, 0xffff0000, v16
	v_fmac_f32_e32 v188, v234, v234
	v_lshlrev_b32_e32 v246, 16, v40
	v_and_b32_e32 v247, 0xffff0000, v40
	v_lshlrev_b32_e32 v248, 16, v41
	v_and_b32_e32 v249, 0xffff0000, v41
	v_lshlrev_b32_e32 v250, 16, v42
	v_and_b32_e32 v251, 0xffff0000, v42
	v_lshlrev_b32_e32 v252, 16, v43
	v_and_b32_e32 v253, 0xffff0000, v43
	global_load_dwordx4 v[106:109], v118, s[4:5] offset:16
	global_load_dwordx4 v[114:117], v118, s[4:5]
	global_load_dwordx4 v[94:97], v118, s[4:5] offset:80
	global_load_dwordx4 v[98:101], v118, s[4:5] offset:64
	global_load_dwordx4 v[86:89], v118, s[4:5] offset:144
	global_load_dwordx4 v[90:93], v118, s[4:5] offset:128
	global_load_dwordx4 v[74:77], v118, s[4:5] offset:208
	global_load_dwordx4 v[78:81], v118, s[4:5] offset:192
	global_load_dwordx4 v[62:65], v118, s[4:5] offset:272
	global_load_dwordx4 v[66:69], v118, s[4:5] offset:256
	global_load_dwordx4 v[54:57], v118, s[4:5] offset:336
	global_load_dwordx4 v[58:61], v118, s[4:5] offset:320
	global_load_dwordx4 v[46:49], v118, s[4:5] offset:400
	global_load_dwordx4 v[50:53], v118, s[4:5] offset:384
	global_load_dwordx4 v[38:41], v118, s[4:5] offset:464
	global_load_dwordx4 v[42:45], v118, s[4:5] offset:448
	v_lshlrev_b32_e32 v236, 16, v17
	v_fmac_f32_e32 v188, v235, v235
	v_and_b32_e32 v237, 0xffff0000, v17
	v_fmac_f32_e32 v188, v236, v236
	v_lshlrev_b32_e32 v238, 16, v10
	v_fmac_f32_e32 v188, v237, v237
	v_and_b32_e32 v239, 0xffff0000, v10
	v_fmac_f32_e32 v188, v238, v238
	v_lshlrev_b32_e32 v240, 16, v11
	v_fmac_f32_e32 v188, v239, v239
	v_and_b32_e32 v241, 0xffff0000, v11
	v_fmac_f32_e32 v188, v240, v240
	v_lshlrev_b32_e32 v242, 16, v12
	v_fmac_f32_e32 v188, v241, v241
	v_and_b32_e32 v243, 0xffff0000, v12
	v_fmac_f32_e32 v188, v242, v242
	v_lshlrev_b32_e32 v244, 16, v13
	v_fmac_f32_e32 v188, v243, v243
	v_and_b32_e32 v245, 0xffff0000, v13
	v_fmac_f32_e32 v188, v244, v244
	v_fmac_f32_e32 v188, v245, v245
	v_fmac_f32_e32 v188, v246, v246
	v_fmac_f32_e32 v188, v247, v247
	v_fmac_f32_e32 v188, v248, v248
	v_fmac_f32_e32 v188, v249, v249
	v_fmac_f32_e32 v188, v250, v250
	v_fmac_f32_e32 v188, v251, v251
	v_fmac_f32_e32 v188, v252, v252
	v_lshlrev_b32_e32 v187, 16, v82
	v_lshlrev_b32_e32 v186, 16, v70
	v_fmac_f32_e32 v188, v253, v253
	v_lshlrev_b32_e32 v124, 16, v144
	v_and_b32_e32 v126, 0xffff0000, v144
	v_lshlrev_b32_e32 v131, 16, v139
	v_and_b32_e32 v133, 0xffff0000, v139
	v_lshlrev_b32_e32 v137, 16, v138
	v_lshlrev_b32_e32 v136, 16, v142
	v_and_b32_e32 v139, 0xffff0000, v138
	v_and_b32_e32 v138, 0xffff0000, v142
	v_lshlrev_b32_e32 v142, 16, v73
	v_and_b32_e32 v144, 0xffff0000, v73
	v_lshlrev_b32_e32 v152, 16, v72
	v_and_b32_e32 v154, 0xffff0000, v72
	v_mul_f32_e32 v72, v186, v186
	v_mul_f32_e32 v73, v187, v187
	s_waitcnt vmcnt(18)
	v_mov_b32_e32 v150, v158
	v_mov_b32_e32 v158, v156
	v_lshlrev_b32_e32 v156, 16, v71
	v_and_b32_e32 v184, 0xffff0000, v71
	v_and_b32_e32 v189, 0xffff0000, v82
	v_add_f32_e32 v71, v73, v188
	v_and_b32_e32 v188, 0xffff0000, v70
	v_mov_b32_e32 v128, v110
	v_mov_b32_e32 v129, v2
	v_mov_b32_e32 v2, v111
	s_waitcnt vmcnt(17)
	v_mov_b32_e32 v151, v20
	v_mov_b32_e32 v20, v159
	v_mov_b32_e32 v159, v18
	v_mov_b32_e32 v18, v157
	v_lshlrev_b32_e32 v157, 16, v83
	v_mul_f32_e32 v110, v188, v188
	v_mul_f32_e32 v111, v189, v189
	v_lshlrev_b32_e32 v119, 16, v141
	v_and_b32_e32 v121, 0xffff0000, v141
	v_lshlrev_b32_e32 v125, 16, v140
	v_and_b32_e32 v127, 0xffff0000, v140
	v_mov_b32_e32 v140, v102
	v_mov_b32_e32 v141, v6
	v_mov_b32_e32 v6, v103
	v_mul_f32_e32 v102, v156, v156
	v_mul_f32_e32 v103, v157, v157
	v_and_b32_e32 v185, 0xffff0000, v83
	v_add_f32_e32 v70, v111, v71
	v_mov_b32_e32 v134, v104
	v_mov_b32_e32 v135, v8
	v_mov_b32_e32 v8, v105
	v_lshlrev_b32_e32 v153, 16, v84
	v_mul_f32_e32 v104, v184, v184
	v_mul_f32_e32 v105, v185, v185
	v_add_f32_e32 v70, v103, v70
	v_mul_f32_e32 v180, v152, v152
	v_mul_f32_e32 v181, v153, v153
	v_and_b32_e32 v155, 0xffff0000, v84
	v_add_f32_e32 v70, v105, v70
	v_lshlrev_b32_e32 v130, 16, v143
	v_and_b32_e32 v132, 0xffff0000, v143
	v_lshlrev_b32_e32 v143, 16, v85
	v_mul_f32_e32 v182, v154, v154
	v_mul_f32_e32 v183, v155, v155
	v_add_f32_e32 v70, v181, v70
	v_lshlrev_b32_e32 v118, 16, v145
	v_and_b32_e32 v120, 0xffff0000, v145
	v_mul_f32_e32 v176, v142, v142
	v_mul_f32_e32 v177, v143, v143
	v_and_b32_e32 v145, 0xffff0000, v85
	v_add_f32_e32 v70, v183, v70
	v_mul_f32_e32 v178, v144, v144
	v_mul_f32_e32 v179, v145, v145
	v_add_f32_e32 v70, v177, v70
	v_mul_f32_e32 v172, v136, v136
	v_mul_f32_e32 v173, v137, v137
	v_add_f32_e32 v70, v179, v70
	v_mul_f32_e32 v174, v138, v138
	v_mul_f32_e32 v175, v139, v139
	v_add_f32_e32 v70, v173, v70
	v_add_f32_e32 v70, v175, v70
	v_fmac_f32_e32 v70, v131, v131
	v_fmac_f32_e32 v70, v133, v133
	v_fmac_f32_e32 v70, v125, v125
	v_fmac_f32_e32 v70, v127, v127
	v_fmac_f32_e32 v70, v119, v119
	v_fmac_f32_e32 v70, v121, v121
	v_add_f32_e32 v103, v72, v70
	v_add_f32_e32 v103, v110, v103
	v_add_f32_e32 v102, v102, v103
	v_add_f32_e32 v173, v104, v102
	v_add_f32_e32 v173, v180, v173
	v_add_f32_e32 v173, v182, v173
	v_add_f32_e32 v173, v176, v173
	v_add_f32_e32 v173, v178, v173
	v_mov_b32_e32 v176, v132
	v_mov_b32_e32 v177, v130
	s_waitcnt vmcnt(16)
	v_mov_b32_e32 v179, v24
	v_add_f32_e32 v24, v172, v173
	v_lshlrev_b64 v[10:11], 8, v[30:31]
	v_mul_f32_e32 v176, v176, v176
	v_mul_f32_e32 v177, v177, v177
	v_add_f32_e32 v24, v174, v24
	v_lshl_add_u64 v[10:11], s[10:11], 0, v[10:11]
	v_lshlrev_b32_e32 v12, 6, v169
	v_mov_b32_e32 v13, v149
	v_mov_b32_e32 v180, v126
	v_mov_b32_e32 v181, v124
	v_add_f32_e32 v24, v177, v24
	v_lshl_add_u64 v[170:171], v[10:11], 0, v[12:13]
	v_mul_f32_e32 v180, v180, v180
	v_mul_f32_e32 v181, v181, v181
	v_add_f32_e32 v24, v176, v24
	global_load_dwordx4 v[10:13], v[170:171], off offset:48
	global_load_dwordx4 v[14:17], v[170:171], off offset:32
	global_load_dwordx4 v[30:33], v[170:171], off offset:16
	global_load_dwordx4 v[34:37], v[170:171], off
	v_mov_b32_e32 v122, v112
	v_mov_b32_e32 v123, v4
	v_mov_b32_e32 v4, v113
	global_load_dwordx4 v[70:73], v[170:171], off offset:176
	global_load_dwordx4 v[82:85], v[170:171], off offset:160
	global_load_dwordx4 v[102:105], v[170:171], off offset:144
	global_load_dwordx4 v[110:113], v[170:171], off offset:128
	v_mov_b32_e32 v170, v120
	v_mov_b32_e32 v171, v118
	v_add_f32_e32 v24, v181, v24
	v_mul_f32_e32 v170, v170, v170
	v_mul_f32_e32 v171, v171, v171
	v_add_f32_e32 v24, v180, v24
	v_add_f32_e32 v24, v171, v24
	v_add_f32_e32 v24, v170, v24
	v_mov_b32_e32 v178, v28
	v_mov_b32_e32 v28, v24
	s_nop 1
	v_permlane32_swap_b32_e32 v24, v28
	v_add_f32_e32 v24, v24, v28
	v_fmamk_f32 v24, v24, 0x3baaaaab, v163
	v_mul_f32_e32 v28, 0x4b800000, v24
	v_cmp_gt_f32_e32 vcc, s69, v24
	s_nop 1
	v_cndmask_b32_e32 v24, v24, v28, vcc
	v_rsq_f32_e32 v170, v24
	v_mov_b32_e32 v24, v29
	v_mov_b32_e32 v29, v22
	v_mov_b32_e32 v28, v26
	v_mul_f32_e32 v22, 0x45800000, v170
	v_cndmask_b32_e32 v22, v170, v22, vcc
	v_mul_f32_e32 v26, 0x3dd53b94, v22
	s_waitcnt vmcnt(22)
	v_mul_f32_e32 v22, v114, v26
	v_mul_f32_e32 v114, v22, v190
	v_mul_f32_e32 v22, v106, v26
	v_mul_f32_e32 v106, v22, v194
	v_mul_f32_e32 v22, v115, v26
	v_mul_f32_e32 v115, v22, v191
	v_mul_f32_e32 v22, v107, v26
	v_mul_f32_e32 v107, v22, v195
	v_mul_f32_e32 v22, v116, v26
	v_mul_f32_e32 v116, v22, v192
	v_mul_f32_e32 v22, v108, v26
	v_mul_f32_e32 v108, v22, v196
	v_mul_f32_e32 v22, v117, v26
	v_mul_f32_e32 v117, v22, v193
	v_mul_f32_e32 v22, v109, v26
	v_mul_f32_e32 v109, v22, v197
	s_waitcnt vmcnt(20)
	v_mul_f32_e32 v22, v98, v26
	v_mul_f32_e32 v170, v22, v198
	v_mul_f32_e32 v22, v94, v26
	v_mul_f32_e32 v94, v22, v202
	v_mul_f32_e32 v22, v99, v26
	v_mul_f32_e32 v171, v22, v199
	v_mul_f32_e32 v22, v95, v26
	v_mul_f32_e32 v95, v22, v203
	v_mul_f32_e32 v22, v100, v26
	v_mul_f32_e32 v172, v22, v200
	v_mul_f32_e32 v22, v96, v26
	v_mul_f32_e32 v96, v22, v204
	v_mul_f32_e32 v22, v101, v26
	v_mul_f32_e32 v173, v22, v201
	v_mul_f32_e32 v22, v97, v26
	v_mul_f32_e32 v97, v22, v205
	s_waitcnt vmcnt(18)
	v_mul_f32_e32 v22, v90, v26
	v_mul_f32_e32 v90, v22, v206
	v_mul_f32_e32 v22, v86, v26
	v_mul_f32_e32 v86, v22, v210
	v_mul_f32_e32 v22, v91, v26
	v_mul_f32_e32 v91, v22, v207
	v_mul_f32_e32 v22, v87, v26
	v_mul_f32_e32 v87, v22, v211
	v_mul_f32_e32 v22, v92, v26
	v_mul_f32_e32 v92, v22, v208
	v_mul_f32_e32 v22, v88, v26
	v_mul_f32_e32 v88, v22, v212
	v_mul_f32_e32 v22, v93, v26
	v_mul_f32_e32 v93, v22, v209
	v_mul_f32_e32 v22, v89, v26
	v_mul_f32_e32 v89, v22, v213
	s_waitcnt vmcnt(16)
	v_mul_f32_e32 v22, v78, v26
	v_mul_f32_e32 v78, v22, v214
	v_mul_f32_e32 v22, v74, v26
	v_mul_f32_e32 v74, v22, v218
	v_mul_f32_e32 v22, v79, v26
	v_mul_f32_e32 v79, v22, v215
	v_mul_f32_e32 v22, v75, v26
	v_mul_f32_e32 v75, v22, v219
	v_mul_f32_e32 v22, v80, v26
	v_mul_f32_e32 v80, v22, v216
	v_mul_f32_e32 v22, v76, v26
	v_mul_f32_e32 v76, v22, v220
	v_mul_f32_e32 v22, v81, v26
	v_mul_f32_e32 v81, v22, v217
	v_mul_f32_e32 v22, v77, v26
	v_mul_f32_e32 v77, v22, v221
	s_waitcnt vmcnt(14)
	v_mul_f32_e32 v22, v66, v26
	v_mul_f32_e32 v66, v22, v222
	v_mul_f32_e32 v22, v26, v62
	v_mul_f32_e32 v62, v22, v226
	v_mul_f32_e32 v22, v67, v26
	v_mul_f32_e32 v67, v22, v223
	v_mul_f32_e32 v22, v26, v63
	v_mul_f32_e32 v63, v22, v227
	v_mul_f32_e32 v22, v68, v26
	v_mul_f32_e32 v68, v22, v224
	v_mul_f32_e32 v22, v26, v64
	v_mul_f32_e32 v64, v22, v228
	v_mul_f32_e32 v22, v69, v26
	v_mul_f32_e32 v69, v22, v225
	v_mul_f32_e32 v22, v26, v65
	v_mul_f32_e32 v65, v22, v229
	s_waitcnt vmcnt(12)
	v_mul_f32_e32 v22, v26, v58
	v_mul_f32_e32 v58, v22, v230
	v_mul_f32_e32 v22, v26, v54
	v_mul_f32_e32 v54, v22, v234
	v_mul_f32_e32 v22, v26, v59
	v_mul_f32_e32 v59, v22, v231
	v_mul_f32_e32 v22, v26, v55
	v_mul_f32_e32 v55, v22, v235
	v_mul_f32_e32 v22, v26, v60
	v_mul_f32_e32 v60, v22, v232
	v_mul_f32_e32 v22, v26, v56
	v_mul_f32_e32 v56, v22, v236
	v_mul_f32_e32 v22, v26, v61
	v_mul_f32_e32 v61, v22, v233
	v_mul_f32_e32 v22, v26, v57
	v_mul_f32_e32 v57, v22, v237
	s_waitcnt vmcnt(10)
	v_mul_f32_e32 v22, v26, v50
	v_mul_f32_e32 v174, v22, v238
	v_mul_f32_e32 v22, v26, v46
	v_mul_f32_e32 v175, v22, v242
	v_mul_f32_e32 v22, v26, v51
	v_mul_f32_e32 v176, v22, v239
	v_mul_f32_e32 v22, v26, v47
	v_mul_f32_e32 v177, v22, v243
	v_mul_f32_e32 v22, v26, v52
	v_mul_f32_e32 v52, v22, v240
	v_mul_f32_e32 v22, v26, v48
	v_mul_f32_e32 v180, v22, v244
	v_mul_f32_e32 v22, v26, v53
	v_mul_f32_e32 v53, v22, v241
	v_mul_f32_e32 v22, v26, v49
	v_mul_f32_e32 v181, v22, v245
	s_waitcnt vmcnt(8)
	v_mul_f32_e32 v22, v26, v42
	v_mul_f32_e32 v182, v22, v246
	v_mul_f32_e32 v22, v26, v38
	v_mul_f32_e32 v183, v22, v250
	v_mul_f32_e32 v22, v26, v43
	v_mul_f32_e32 v190, v22, v247
	v_mul_f32_e32 v22, v26, v39
	v_mul_f32_e32 v191, v22, v251
	v_mul_f32_e32 v22, v26, v44
	v_mul_f32_e32 v192, v22, v248
	v_mul_f32_e32 v22, v26, v40
	v_mul_f32_e32 v193, v22, v252
	v_mul_f32_e32 v22, v26, v45
	v_mul_f32_e32 v194, v22, v249
	v_mul_f32_e32 v22, v26, v41
	v_mul_f32_e32 v28, v26, v28
	v_mul_f32_e32 v29, v26, v29
	v_mul_f32_e32 v195, v22, v253
	v_mul_f32_e32 v28, v28, v186
	v_mul_f32_e32 v29, v29, v187
	v_mov_b32_e32 v22, v27
	v_mul_f32_e32 v38, v26, v158
	v_mul_f32_e32 v39, v26, v159
	v_mul_f32_e32 v22, v26, v22
	v_mul_f32_e32 v23, v26, v23
	v_mul_f32_e32 v18, v26, v18
	v_mul_f32_e32 v19, v26, v19
	v_mul_f32_e32 v40, v26, v178
	v_mul_f32_e32 v41, v26, v179
	v_mul_f32_e32 v42, v26, v150
	v_mul_f32_e32 v43, v26, v151
	v_mul_f32_e32 v24, v26, v24
	v_mul_f32_e32 v25, v26, v25
	v_mul_f32_e32 v20, v26, v20
	v_mul_f32_e32 v21, v26, v21
	v_mul_f32_e32 v44, v26, v140
	v_mul_f32_e32 v45, v26, v141
	v_mul_f32_e32 v46, v26, v128
	v_mul_f32_e32 v47, v26, v129
	v_mul_f32_e32 v6, v26, v6
	v_mul_f32_e32 v7, v26, v7
	v_mul_f32_e32 v2, v26, v2
	v_mul_f32_e32 v3, v26, v3
	v_mul_f32_e32 v48, v26, v134
	v_mul_f32_e32 v49, v26, v135
	v_mul_f32_e32 v50, v26, v122
	v_mul_f32_e32 v51, v26, v123
	v_mul_f32_e32 v8, v26, v8
	v_mul_f32_e32 v9, v26, v9
	v_mul_f32_e32 v4, v26, v4
	v_mul_f32_e32 v5, v26, v5
	s_waitcnt vmcnt(4)
	v_mul_f32_e32 v26, v29, v34
	v_mul_f32_e32 v27, v28, v35
	v_mul_f32_e32 v22, v22, v188
	v_mul_f32_e32 v23, v23, v189
	v_mul_f32_e32 v48, v48, v130
	v_mul_f32_e32 v49, v49, v131
	v_sub_f32_e32 v130, v26, v27
	v_mul_f32_e32 v26, v28, v34
	v_mul_f32_e32 v27, v29, v35
	v_mul_f32_e32 v40, v40, v156
	v_mul_f32_e32 v41, v41, v157
	v_add_f32_e32 v28, v27, v26
	v_mul_f32_e32 v26, v23, v36
	v_mul_f32_e32 v27, v22, v37
	v_mul_f32_e32 v22, v22, v36
	v_mul_f32_e32 v23, v23, v37
	v_sub_f32_e32 v26, v26, v27
	v_add_f32_e32 v27, v23, v22
	v_mul_f32_e32 v22, v41, v30
	v_mul_f32_e32 v23, v40, v31
	v_mul_f32_e32 v24, v24, v184
	v_mul_f32_e32 v25, v25, v185
	v_sub_f32_e32 v29, v22, v23
	v_mul_f32_e32 v22, v40, v30
	v_mul_f32_e32 v23, v41, v31
	v_mul_f32_e32 v38, v38, v152
	v_mul_f32_e32 v39, v39, v153
	v_add_f32_e32 v30, v23, v22
	v_mul_f32_e32 v22, v25, v32
	v_mul_f32_e32 v23, v24, v33
	v_sub_f32_e32 v31, v22, v23
	v_mul_f32_e32 v22, v24, v32
	v_mul_f32_e32 v23, v25, v33
	v_mul_f32_e32 v18, v18, v154
	v_mul_f32_e32 v19, v19, v155
	v_add_f32_e32 v24, v23, v22
	v_mul_f32_e32 v22, v39, v14
	v_mul_f32_e32 v23, v38, v15
	v_mul_f32_e32 v14, v38, v14
	v_mul_f32_e32 v15, v39, v15
	v_sub_f32_e32 v22, v22, v23
	v_add_f32_e32 v23, v15, v14
	v_mul_f32_e32 v14, v19, v16
	v_mul_f32_e32 v15, v18, v17
	v_mul_f32_e32 v42, v42, v142
	v_mul_f32_e32 v43, v43, v143
	v_sub_f32_e32 v25, v14, v15
	v_mul_f32_e32 v14, v18, v16
	v_mul_f32_e32 v15, v19, v17
	v_mul_f32_e32 v20, v20, v144
	v_mul_f32_e32 v21, v21, v145
	v_add_f32_e32 v16, v15, v14
	v_mul_f32_e32 v14, v43, v10
	v_mul_f32_e32 v15, v42, v11
	v_mul_f32_e32 v10, v42, v10
	v_mul_f32_e32 v11, v43, v11
	v_sub_f32_e32 v14, v14, v15
	v_add_f32_e32 v15, v11, v10
	v_mul_f32_e32 v10, v21, v12
	v_mul_f32_e32 v11, v20, v13
	v_mul_f32_e32 v44, v44, v136
	v_mul_f32_e32 v45, v45, v137
	v_sub_f32_e32 v17, v10, v11
	v_mul_f32_e32 v10, v20, v12
	v_mul_f32_e32 v11, v21, v13
	v_mul_f32_e32 v6, v6, v138
	v_mul_f32_e32 v7, v7, v139
	v_add_f32_e32 v12, v11, v10
	s_waitcnt vmcnt(0)
	v_mul_f32_e32 v10, v45, v110
	v_mul_f32_e32 v11, v44, v111
	v_sub_f32_e32 v13, v10, v11
	v_mul_f32_e32 v10, v44, v110
	v_mul_f32_e32 v11, v45, v111
	v_mul_f32_e32 v8, v8, v132
	v_mul_f32_e32 v9, v9, v133
	v_add_f32_e32 v18, v11, v10
	v_mul_f32_e32 v10, v7, v112
	v_mul_f32_e32 v11, v6, v113
	v_mul_f32_e32 v6, v6, v112
	v_mul_f32_e32 v7, v7, v113
	v_sub_f32_e32 v10, v10, v11
	v_add_f32_e32 v11, v7, v6
	v_mul_f32_e32 v6, v49, v102
	v_mul_f32_e32 v7, v48, v103
	v_sub_f32_e32 v19, v6, v7
	v_mul_f32_e32 v6, v48, v102
	v_mul_f32_e32 v7, v49, v103
	v_mul_f32_e32 v46, v46, v124
	v_mul_f32_e32 v47, v47, v125
	v_add_f32_e32 v20, v7, v6
	v_mul_f32_e32 v6, v9, v104
	v_mul_f32_e32 v7, v8, v105
	v_sub_f32_e32 v21, v6, v7
	v_mul_f32_e32 v6, v8, v104
	v_mul_f32_e32 v7, v9, v105
	v_mul_f32_e32 v2, v2, v126
	v_mul_f32_e32 v3, v3, v127
	v_add_f32_e32 v8, v7, v6
	v_mul_f32_e32 v6, v47, v82
	v_mul_f32_e32 v7, v46, v83
	v_sub_f32_e32 v9, v6, v7
	v_mul_f32_e32 v6, v46, v82
	v_mul_f32_e32 v7, v47, v83
	v_mul_f32_e32 v50, v50, v118
	v_mul_f32_e32 v51, v51, v119
	v_add_f32_e32 v32, v7, v6
	v_mul_f32_e32 v6, v3, v84
	v_mul_f32_e32 v7, v2, v85
	v_mul_f32_e32 v2, v2, v84
	v_mul_f32_e32 v3, v3, v85
	v_sub_f32_e32 v6, v6, v7
	v_add_f32_e32 v7, v3, v2
	v_mul_f32_e32 v2, v51, v70
	v_mul_f32_e32 v3, v50, v71
	v_mul_f32_e32 v4, v4, v120
	v_mul_f32_e32 v5, v5, v121
	v_sub_f32_e32 v33, v2, v3
	v_mul_f32_e32 v2, v50, v70
	v_mul_f32_e32 v3, v51, v71
	v_cvt_pk_bf16_f32 v98, v114, v115
	v_cvt_pk_bf16_f32 v99, v116, v117
	v_cvt_pk_bf16_f32 v100, v106, v107
	v_cvt_pk_bf16_f32 v101, v108, v109
	v_cvt_pk_bf16_f32 v102, v170, v171
	s_nop 0
	v_add_f32_e32 v34, v3, v2
	v_mul_f32_e32 v2, v5, v72
	v_mul_f32_e32 v3, v4, v73
	v_sub_f32_e32 v35, v2, v3
	v_mul_f32_e32 v2, v4, v72
	v_mul_f32_e32 v3, v5, v73
	v_cvt_pk_bf16_f32 v103, v172, v173
	v_cvt_pk_bf16_f32 v104, v94, v95
	v_cvt_pk_bf16_f32 v105, v96, v97
	v_cvt_pk_bf16_f32 v106, v90, v91
	v_cvt_pk_bf16_f32 v107, v92, v93
	s_nop 0
	v_add_f32_e32 v2, v3, v2
	v_cvt_pk_bf16_f32 v108, v86, v87
	v_cvt_pk_bf16_f32 v109, v88, v89
	v_cvt_pk_bf16_f32 v110, v78, v79
	v_cvt_pk_bf16_f32 v111, v80, v81
	v_cvt_pk_bf16_f32 v112, v74, v75
	v_cvt_pk_bf16_f32 v113, v76, v77
	v_cvt_pk_bf16_f32 v114, v66, v67
	v_cvt_pk_bf16_f32 v115, v68, v69
	v_cvt_pk_bf16_f32 v116, v62, v63
	v_cvt_pk_bf16_f32 v117, v64, v65
	v_cvt_pk_bf16_f32 v118, v58, v59
	v_cvt_pk_bf16_f32 v119, v60, v61
	v_cvt_pk_bf16_f32 v120, v54, v55
	v_cvt_pk_bf16_f32 v121, v56, v57
	v_cvt_pk_bf16_f32 v122, v174, v176
	v_cvt_pk_bf16_f32 v123, v52, v53
	v_cvt_pk_bf16_f32 v124, v175, v177
	v_cvt_pk_bf16_f32 v125, v180, v181
	v_cvt_pk_bf16_f32 v126, v182, v190
	v_cvt_pk_bf16_f32 v127, v192, v194
	v_cvt_pk_bf16_f32 v128, v183, v191
	v_cvt_pk_bf16_f32 v129, v193, v195
	v_cvt_pk_bf16_f32 v130, v130, v26
	v_cvt_pk_bf16_f32 v131, v29, v31
	v_cvt_pk_bf16_f32 v132, v22, v25
	v_cvt_pk_bf16_f32 v133, v14, v17
	v_cvt_pk_bf16_f32 v134, v13, v10
	v_cvt_pk_bf16_f32 v135, v19, v21
	v_cvt_pk_bf16_f32 v136, v9, v6
	v_cvt_pk_bf16_f32 v137, v33, v35
	v_cvt_pk_bf16_f32 v138, v28, v27
	v_cvt_pk_bf16_f32 v139, v30, v24
	v_cvt_pk_bf16_f32 v140, v23, v16
	v_cvt_pk_bf16_f32 v141, v15, v12
	v_cvt_pk_bf16_f32 v142, v18, v11
	v_cvt_pk_bf16_f32 v143, v20, v8
	v_cvt_pk_bf16_f32 v144, v32, v7
	v_cvt_pk_bf16_f32 v145, v34, v2
	v_mul_hi_i32 v2, v168, s70
	v_lshrrev_b32_e32 v3, 31, v2
	v_ashrrev_i32_e32 v2, 2, v2
	v_add_u32_e32 v2, v2, v3
	v_mul_lo_u32 v3, v2, 24
	v_sub_u32_e32 v3, v168, v3
	v_lshrrev_b32_e32 v16, 1, v2
	v_bitop3_b32 v3, v16, v3, 7 bitop3:0x6c
	v_mul_lo_u32 v2, v2, s68
	v_lshl_add_u32 v2, v3, 4, v2
	v_add_u32_e32 v3, 0x200, v168
	v_mul_hi_i32 v4, v3, s70
	v_lshrrev_b32_e32 v5, 31, v4
	v_ashrrev_i32_e32 v4, 2, v4
	v_add_u32_e32 v4, v4, v5
	v_mul_lo_u32 v5, v4, 24
	v_sub_u32_e32 v5, v3, v5
	v_lshrrev_b32_e32 v16, 1, v4
	v_bitop3_b32 v5, v16, v5, 7 bitop3:0x6c
	v_mul_lo_u32 v4, v4, s68
	v_lshl_add_u32 v4, v5, 4, v4
	v_add_u32_e32 v5, 0x400, v168
	v_mul_hi_i32 v6, v5, s70
	v_lshrrev_b32_e32 v7, 31, v6
	v_ashrrev_i32_e32 v6, 2, v6
	v_add_u32_e32 v6, v6, v7
	v_mul_lo_u32 v7, v6, 24
	v_sub_u32_e32 v5, v5, v7
	v_lshrrev_b32_e32 v16, 1, v6
	v_bitop3_b32 v5, v16, v5, 7 bitop3:0x6c
	v_mul_lo_u32 v6, v6, s68
	v_ashrrev_i32_e32 v9, 4, v168
	v_lshl_add_u32 v6, v5, 4, v6
	v_bfe_u32 v5, v168, 2, 2
	v_lshrrev_b32_e32 v7, 1, v168
	v_and_b32_e32 v10, 0x1ffff0, v9
	v_lshrrev_b32_e32 v9, 1, v9
	v_ashrrev_i32_e32 v3, 4, v3
	v_and_or_b32 v5, v7, 8, v5
	v_and_b32_e32 v7, 0x60, v168
	v_lshlrev_b32_e32 v8, 3, v168
	v_and_b32_e32 v9, 4, v9
	v_and_b32_e32 v11, 0x1ffff0, v3
	v_lshrrev_b32_e32 v3, 1, v3
	v_and_or_b32 v7, v8, 24, v7
	v_or3_b32 v9, v10, v9, v5
	v_and_b32_e32 v3, 4, v3
	s_barrier
	global_load_lds_dwordx4 v2, s[44:45]
	s_mov_b32 m0, s72
	v_lshlrev_b32_e32 v7, 1, v7
	v_lshlrev_b32_e32 v10, 11, v9
	v_or3_b32 v3, v11, v3, v5
	global_load_lds_dwordx4 v4, s[44:45]
	s_mov_b32 m0, s73
	v_or_b32_e32 v9, v10, v7
	v_lshlrev_b32_e32 v11, 11, v3
	global_load_lds_dwordx4 v6, s[44:45]
	s_mov_b32 m0, s64
	v_or_b32_e32 v3, v11, v7
	global_load_lds_dwordx4 v9, s[46:47]
	s_mov_b32 m0, s74
	v_lshlrev_b32_e32 v13, 1, v168
	global_load_lds_dwordx4 v3, s[46:47]
	v_lshlrev_b32_e32 v9, 4, v168
	v_and_b32_e32 v14, 32, v13
	v_or_b32_e32 v3, 32, v148
	v_and_b32_e32 v16, 0x13, v167
	v_and_b32_e32 v17, 4, v167
	v_lshl_or_b32 v16, v17, 1, v16
	v_and_b32_e32 v17, 8, v167
	v_lshrrev_b32_e32 v17, 1, v17
	v_or_b32_e32 v16, v16, v17
	v_mul_u32_u24_e32 v5, 0x180, v16
	v_lshlrev_b32_e32 v17, 3, v16
	v_and_b32_e32 v7, 0x70, v17
	v_and_b32_e32 v12, 0xc0, v9
	v_and_or_b32 v8, v8, s75, v14
	v_bitop3_b32 v172, v3, v5, v7 bitop3:0xde
	v_or_b32_e32 v3, 64, v148
	v_mul_i32_i24_e32 v15, -8, v169
	v_add3_u32 v169, v12, 0, v8
	v_and_b32_e32 v12, 0xc0, v13
	v_and_b32_e32 v13, 48, v9
	v_bitop3_b32 v173, v3, v5, v7 bitop3:0xde
	v_or_b32_e32 v3, 0x60, v148
	v_or3_b32 v8, v11, v12, v13
	v_mov_b32_e32 v9, v149
	v_bitop3_b32 v171, v148, v5, v7 bitop3:0xde
	v_bitop3_b32 v174, v3, v5, v7 bitop3:0xde
	v_mov_b32_e32 v3, v149
	v_mov_b32_e32 v5, v149
	v_mov_b32_e32 v7, v149
	v_lshl_add_u64 v[150:151], s[48:49], 0, v[8:9]
	v_mov_b32_e32 v240, v8
	v_or3_b32 v8, v10, v12, v13
	v_mov_b32_e32 v16, v149
	v_mov_b32_e32 v17, v149
	v_and_b32_e32 v170, 63, v168
	s_lshl_b32 s46, s80, 2
	v_lshl_add_u32 v168, v167, 2, s65
	v_lshl_add_u64 v[152:153], s[48:49], 0, v[8:9]
	v_mov_b32_e32 v241, v8
	v_lshl_add_u64 v[154:155], s[50:51], 0, v[6:7]
	v_mov_b32_e32 v242, v6
	v_lshl_add_u64 v[156:157], s[50:51], 0, v[4:5]
	v_mov_b32_e32 v243, v4
	v_lshl_add_u64 v[158:159], s[50:51], 0, v[2:3]
	v_mov_b32_e32 v244, v2
	s_add_u32 s94, s2, s50
	s_addc_u32 s95, s3, s51
	s_add_u32 s96, s2, s48
	s_addc_u32 s97, s3, s49
	v_add3_u32 v167, s63, v15, v167
	v_mov_b32_e32 v2, v149
	v_mov_b32_e32 v4, v149
	v_mov_b32_e32 v6, v149
	v_mov_b32_e32 v8, v149
	v_mov_b32_e32 v10, v149
	v_mov_b32_e32 v11, v149
	v_mov_b32_e32 v12, v149
	v_mov_b32_e32 v13, v149
	v_mov_b32_e32 v14, v149
	v_mov_b32_e32 v15, v149
	v_mov_b64_e32 v[32:33], v[16:17]
	v_mov_b64_e32 v[48:49], v[16:17]
	v_mov_b64_e32 v[64:65], v[16:17]
	s_add_i32 s46, s46, 4
	v_cmp_gt_u32_e64 s[0:1], 32, v170
	v_mov_b32_e32 v176, 0
	v_mov_b32_e32 v175, 0
	v_mov_b32_e32 v210, 0
	v_mov_b32_e32 v211, 0
	v_mov_b32_e32 v212, 0
	v_mov_b32_e32 v213, 0
	v_mov_b32_e32 v214, 0
	v_mov_b32_e32 v215, 0
	v_mov_b32_e32 v216, 0
	v_mov_b32_e32 v217, 0
	v_mov_b32_e32 v218, 0
	v_mov_b32_e32 v219, 0
	v_mov_b32_e32 v220, 0
	v_mov_b32_e32 v221, 0
	v_mov_b32_e32 v222, 0
	v_mov_b32_e32 v223, 0
	v_mov_b32_e32 v224, 0
	v_mov_b32_e32 v225, 0
	s_movk_i32 s47, 0xff00
	v_mov_b64_e32 v[30:31], v[14:15]
	v_mov_b64_e32 v[28:29], v[12:13]
	v_mov_b64_e32 v[26:27], v[10:11]
	v_mov_b64_e32 v[24:25], v[8:9]
	v_mov_b64_e32 v[22:23], v[6:7]
	v_mov_b64_e32 v[20:21], v[4:5]
	v_mov_b64_e32 v[18:19], v[2:3]
	v_mov_b64_e32 v[46:47], v[14:15]
	v_mov_b64_e32 v[44:45], v[12:13]
	v_mov_b64_e32 v[42:43], v[10:11]
	v_mov_b64_e32 v[40:41], v[8:9]
	v_mov_b64_e32 v[38:39], v[6:7]
	v_mov_b64_e32 v[36:37], v[4:5]
	v_mov_b64_e32 v[34:35], v[2:3]
	v_mov_b64_e32 v[62:63], v[14:15]
	v_mov_b64_e32 v[60:61], v[12:13]
	v_mov_b64_e32 v[58:59], v[10:11]
	v_mov_b64_e32 v[56:57], v[8:9]
	v_mov_b64_e32 v[54:55], v[6:7]
	v_mov_b64_e32 v[52:53], v[4:5]
	v_mov_b64_e32 v[50:51], v[2:3]
	s_cmp_ge_u32 s64, 0x1000
	s_cbranch_scc0 .Lprio_skip_a2
	s_setprio 1
.Lprio_skip_a2:
.LBB0_946:
	s_add_i32 s44, s12, -1
	s_waitcnt vmcnt(0)
	s_and_b32 s48, s44, 1
	s_cmp_ge_u32 s12, s46
	s_waitcnt vmcnt(0) lgkmcnt(0)
	s_barrier
	s_cbranch_scc1 .LBB0_948
	s_xor_b32 s44, s48, 1
	s_mulk_i32 s44, 0x6000
	s_add_i32 s44, s64, s44
	s_add_i32 m0, s44, 0x8000
	s_nop 0
	global_load_lds_dwordx4 v244, s[94:95]
	s_add_i32 m0, s44, 0xa000
	s_nop 0
	global_load_lds_dwordx4 v243, s[94:95]
	s_add_i32 m0, s44, 0xc000
	s_lshl_b32 s44, s48, 14
	s_xor_b32 s44, s44, 0x4000
	s_add_i32 s44, s64, s44
	global_load_lds_dwordx4 v242, s[94:95]
	s_mov_b32 m0, s44
	s_nop 0
	global_load_lds_dwordx4 v241, s[96:97]
	s_add_i32 m0, s44, 0x2000
	s_nop 0
	global_load_lds_dwordx4 v240, s[96:97]



.LBB0_1087:
	s_setprio 0
	s_mov_b64 s[0:1], s[54:55]
	s_load_dword s2, s[0:1], 0x13c
	s_waitcnt lgkmcnt(0)
	s_cmp_lt_i32 s2, 6
	s_cbranch_scc1 .LBB0_1142
	s_load_dword s0, s[0:1], 0x138
	s_waitcnt lgkmcnt(0)
	s_cmp_gt_i32 s0, 4
	s_cbranch_scc1 .LBB0_1142
	s_mov_b64 s[2:3], s[54:55]
	s_getreg_b32 s4, hwreg(HW_REG_XCC_ID, 0, 4)
	s_waitcnt vmcnt(0)
	v_cmp_eq_u32_e32 vcc, 0, v0
	s_waitcnt vmcnt(0)
	s_barrier
	s_and_saveexec_b64 s[0:1], vcc
	s_cbranch_execz .LBB0_1141
	s_add_i32 s5, 0, 0x22ff0
	v_mov_b32_e32 v1, s5
	s_load_dwordx2 s[2:3], s[2:3], 0x130
	s_waitcnt vmcnt(0) expcnt(0) lgkmcnt(0)
	ds_read_b32 v3, v1
	s_add_i32 s5, 0, 0x22ff4
	v_mov_b32_e32 v1, s5
	ds_read_b32 v1, v1
	s_and_b32 s20, s4, 15
	s_waitcnt lgkmcnt(1)
	v_cmp_ne_u32_e32 vcc, 0, v3
	s_cbranch_vccnz .LBB0_1105
	v_readlane_b32 s4, v254, 0
	v_readlane_b32 s5, v254, 1
	s_load_dwordx2 s[10:11], s[4:5], 0x4
	s_add_u32 s4, s2, 0x1000
	s_addc_u32 s5, s3, 0
	s_add_u32 s6, s2, 0x1100
	s_addc_u32 s7, s3, 0
	s_waitcnt lgkmcnt(0)
	s_mul_i32 s21, s10, s92
	s_add_u32 s10, s2, 0x1200
	s_mul_i32 s21, s21, s11
	s_addc_u32 s11, s3, 0
	s_add_u32 s12, s2, 0x1300
	s_addc_u32 s13, s3, 0
	s_mov_b32 s22, 1
	v_mov_b32_e32 v17, 0
	s_branch .LBB0_1093
